# GEMM K-loops: s_setprio flips removed, one static s_setprio 1 for waves 4-7 per gemm call (reset at grid barriers); phase-E epilogue waits counted per step (vmcnt(7)) instead of one vmcnt(0) per batch
# baseline (speedup 1.0000x reference)
.LBB0_181:
	s_cmpk_gt_i32 s33, 0x40f
	v_readfirstlane_b32 s39, v0
	s_barrier
	s_cbranch_scc1 .LBB0_193
	v_lshlrev_b32_e32 v1, 4, v0
	v_bfe_u32 v2, v0, 3, 25
	v_and_b32_e32 v5, 32, v0
	v_or_b32_e32 v2, 64, v2
	v_bfe_u32 v3, v0, 2, 4
	s_movk_i32 s0, 0x70
	v_bitop3_b32 v1, v1, v5, 48 bitop3:0x6c
	s_add_u32 s40, s6, 0x1170000
	v_and_or_b32 v4, v2, s0, v3
	v_and_or_b32 v1, v0, 64, v1
	s_addc_u32 s41, s7, 0
	v_lshl_or_b32 v132, v4, 9, v1
	v_lshrrev_b32_e32 v4, 5, v0
	v_lshrrev_b32_e32 v6, 1, v0
	s_add_u32 s42, s6, 0x130000
	v_and_b32_e32 v4, 4, v4
	v_bfe_u32 v5, v0, 2, 2
	v_and_b32_e32 v10, 24, v6
	s_addc_u32 s43, s7, 0
	v_or3_b32 v4, v4, v5, v10
	s_movk_i32 s0, 0x60
	s_ashr_i32 s45, s33, 31
	v_and_or_b32 v2, v2, s0, v4
	s_lshr_b32 s0, s45, 29
	s_add_i32 s0, s33, s0
	s_lshr_b32 s2, s39, 6
	s_ashr_i32 s3, s0, 3
	s_and_b32 s0, s0, -8
	s_lshr_b32 s1, s39, 8
	s_lshl_b32 s44, s2, 10
	s_sub_i32 s0, s33, s0
	s_cmp_lt_i32 s0, 0
	s_movk_i32 s46, 0x83
	s_cselect_b32 s8, s46, 0x82
	s_mul_i32 s0, s8, s0
	s_add_i32 s0, s0, s3
	s_mul_hi_i32 s3, s0, 0x7e07e07f
	s_lshr_b32 s8, s3, 31
	s_ashr_i32 s3, s3, 8
	s_add_i32 s3, s3, s8
	s_lshl_b32 s8, s3, 3
	s_mulk_i32 s3, 0x208
	s_sub_i32 s3, s0, s3
	s_bfe_u32 s0, s3, 0x3001c
	s_add_i32 s9, s3, s0
	s_sext_i32_i16 s0, s9
	s_and_b32 s9, s9, 0xfff8
	s_sub_i32 s3, s3, s9
	s_sext_i32_i16 s3, s3
	s_add_i32 s16, s8, s3
	s_ashr_i32 s17, s16, 31
	s_lshr_b32 s0, s0, 3
	s_lshl_b64 s[8:9], s[16:17], 17
	s_add_u32 s18, s40, s8
	s_addc_u32 s19, s41, s9
	s_bfe_i64 s[8:9], s[0:1], 0x100000
	s_lshl_b64 s[8:9], s[8:9], 17
	v_lshl_or_b32 v134, v2, 9, v1
	v_lshrrev_b32_e32 v2, 3, v0
	s_add_u32 s20, s42, s8
	v_and_or_b32 v3, v2, 48, v3
	v_and_or_b32 v2, v2, 32, v4
	s_addc_u32 s21, s43, s9
	s_add_i32 s17, s44, 0
	v_lshl_or_b32 v138, v2, 9, v1
	s_add_i32 m0, s17, 0x10000
	v_lshl_or_b32 v136, v3, 9, v1
	global_load_lds_dwordx4 v138, s[20:21]
	s_add_i32 m0, s17, 0x12000
	s_add_i32 s47, s17, 0x2000
	global_load_lds_dwordx4 v134, s[20:21]
	s_mov_b32 m0, s17
	s_add_u32 s8, s20, 0x10000
	global_load_lds_dwordx4 v136, s[18:19]
	s_mov_b32 m0, s47
	s_addc_u32 s9, s21, 0
	global_load_lds_dwordx4 v132, s[18:19]
	s_add_i32 m0, s17, 0x14000
	v_mov_b32_e32 v139, 0
	global_load_lds_dwordx4 v138, s[8:9]
	s_add_i32 m0, s17, 0x16000
	v_mov_b32_e32 v135, v139
	global_load_lds_dwordx4 v134, s[8:9]
	s_add_u32 s8, s18, 0x10000
	s_addc_u32 s9, s19, 0
	s_add_i32 s48, s17, 0x4000
	s_mov_b32 m0, s48
	s_add_i32 s49, s17, 0x6000
	global_load_lds_dwordx4 v136, s[8:9]
	s_mov_b32 m0, s49
	v_mov_b32_e32 v137, v139
	global_load_lds_dwordx4 v132, s[8:9]
	v_mov_b32_e32 v133, v139
	s_mov_b32 s50, 0
	v_lshl_add_u64 v[8:9], s[20:21], 0, v[138:139]
	v_lshl_add_u64 v[6:7], s[20:21], 0, v[134:135]
	v_lshl_add_u64 v[4:5], s[18:19], 0, v[136:137]
	s_cmp_lg_u32 s1, 1
	v_lshl_add_u64 v[2:3], s[18:19], 0, v[132:133]
	s_cbranch_scc1 .LBB0_184
	s_barrier
	s_setprio 1

.LBB0_303:
	s_andn2_b64 vcc, exec, s[6:7]
	s_cbranch_vccnz .LBB0_376
	v_lshrrev_b32_e32 v3, 1, v0
	s_waitcnt vmcnt(8)
	v_and_b32_e32 v14, 24, v3
	v_lshrrev_b32_e32 v3, 5, v0
	v_lshlrev_b32_e32 v1, 4, v0
	v_and_b32_e32 v2, 32, v0
	v_and_b32_e32 v3, 4, v3
	v_bfe_u32 v4, v0, 2, 2
	s_add_u32 s38, s16, 0x11f40000
	v_bfe_u32 v12, v0, 2, 4
	v_bitop3_b32 v10, v1, v2, 48 bitop3:0x6c
	v_and_b32_e32 v11, 64, v0
	v_or3_b32 v3, v3, v4, v14
	v_lshrrev_b32_e32 v4, 3, v0
	v_or_b32_e32 v13, 0x2000, v1
	s_addc_u32 s39, s17, 0
	v_or_b32_e32 v2, v10, v11
	v_and_or_b32 v5, v4, 48, v12
	v_and_or_b32 v4, v4, 32, v3
	v_lshrrev_b32_e32 v1, 7, v13
	s_movk_i32 s1, 0x70
	s_add_u32 s40, s16, 0x3af40000
	v_lshl_or_b32 v134, v4, 12, v2
	v_and_or_b32 v4, v1, s1, v12
	s_movk_i32 s1, 0x60
	s_addc_u32 s41, s17, 0
	v_and_or_b32 v1, v1, s1, v3
	s_lshr_b32 s6, s37, 6
	s_ashr_i32 s1, s0, 31
	s_lshr_b32 s8, s37, 8
	s_lshl_b32 s42, s6, 10
	s_ashr_i32 s7, s34, 31
	s_add_i32 s9, s34, 0xfffffc18
	s_lshl_b64 s[4:5], s[0:1], 20
	s_add_u32 s1, s40, s4
	s_addc_u32 s10, s41, s5
	s_add_u32 s4, s38, s4
	s_addc_u32 s5, s39, s5
	s_add_u32 s11, s4, 0xc00000
	s_addc_u32 s12, s5, 0
	s_cmpk_gt_i32 s34, 0x3e7
	s_cselect_b32 s5, 0, s7
	s_cselect_b32 s4, s9, s34
	s_cselect_b32 s7, s39, s41
	s_cselect_b32 s9, s38, s40
	s_cselect_b32 s28, s1, s11
	s_cselect_b32 s29, s10, s12
	s_lshl_b64 s[4:5], s[4:5], 20
	s_add_u32 s26, s9, s4
	s_addc_u32 s27, s7, s5
	s_add_i32 s43, s42, 0
	s_add_i32 m0, s43, 0x10000
	v_lshl_or_b32 v138, v1, 12, v2
	global_load_lds_dwordx4 v134, s[28:29]
	s_add_i32 m0, s43, 0x12000
	v_lshl_or_b32 v136, v5, 12, v2
	global_load_lds_dwordx4 v138, s[28:29]
	s_mov_b32 m0, s43
	s_add_i32 s44, s43, 0x2000
	v_lshl_or_b32 v140, v4, 12, v2
	global_load_lds_dwordx4 v136, s[26:27]
	s_mov_b32 m0, s44
	s_add_u32 s4, s28, 0x80000
	global_load_lds_dwordx4 v140, s[26:27]
	s_addc_u32 s5, s29, 0
	s_add_i32 m0, s43, 0x14000
	v_mov_b32_e32 v135, 0
	global_load_lds_dwordx4 v134, s[4:5]
	s_add_i32 m0, s43, 0x16000
	v_mov_b32_e32 v139, v135
	global_load_lds_dwordx4 v138, s[4:5]
	s_add_u32 s4, s26, 0x80000
	s_addc_u32 s5, s27, 0
	s_add_i32 s45, s43, 0x4000
	s_mov_b32 m0, s45
	s_add_i32 s46, s43, 0x6000
	global_load_lds_dwordx4 v136, s[4:5]
	s_mov_b32 m0, s46
	v_mov_b32_e32 v137, v135
	global_load_lds_dwordx4 v140, s[4:5]
	v_mov_b32_e32 v141, v135
	s_mov_b32 s47, 0
	v_lshl_add_u64 v[8:9], s[28:29], 0, v[134:135]
	v_lshl_add_u64 v[6:7], s[28:29], 0, v[138:139]
	v_lshl_add_u64 v[4:5], s[26:27], 0, v[136:137]
	s_cmp_lg_u32 s8, 1
	v_lshl_add_u64 v[2:3], s[26:27], 0, v[140:141]
	s_cbranch_scc1 .LBB0_306
	s_barrier
	s_setprio 1

.LBB0_1191:
	s_cmp_lt_i32 s54, 7
	s_cselect_b64 s[4:5], -1, 0
	s_and_b64 s[0:1], s[4:5], s[0:1]
	s_andn2_b64 vcc, exec, s[0:1]
	s_cbranch_vccnz .LBB0_1229
	v_mov_b32_e32 v1, v248
	s_waitcnt vmcnt(11)
	v_mov_b32_e32 v2, v0
	v_readlane_b32 s30, v250, 1
	v_readlane_b32 s31, v250, 0
	v_readlane_b32 s0, v250, 39
	s_mov_b64 s[0:1], s[90:91]
	s_mov_b64 s[6:7], s[52:53]
	v_lshlrev_b32_e32 v2, 4, v0
	v_and_b32_e32 v1, 32, v0
	v_or_b32_e32 v150, 0x2000, v2
	v_bfe_u32 v149, v0, 2, 4
	v_bitop3_b32 v1, v2, v1, 48 bitop3:0x6c
	v_and_b32_e32 v148, 64, v0
	v_lshrrev_b32_e32 v4, 3, v0
	v_lshrrev_b32_e32 v2, 7, v150
	s_movk_i32 s0, 0x70
	v_or_b32_e32 v3, v1, v148
	v_and_or_b32 v4, v4, 48, v149
	v_and_or_b32 v2, v2, s0, v149
	v_lshl_or_b32 v130, v4, 11, v3
	v_lshl_or_b32 v132, v2, 11, v3
	v_bfe_u32 v151, v0, 4, 2
	v_lshlrev_b32_e32 v2, 6, v0
	v_lshlrev_b32_e32 v3, 2, v0
	v_lshlrev_b32_e32 v153, 4, v151
	v_and_b32_e32 v2, 0x3c0, v2
	v_and_b32_e32 v3, 32, v3
	s_cmpk_lt_i32 s31, 0x208
	v_readfirstlane_b32 s33, v0
	v_and_b32_e32 v152, 15, v0
	s_cselect_b64 s[2:3], -1, 0
	s_cmpk_gt_i32 s31, 0x207
	v_bitop3_b32 v154, v153, v3, v2 bitop3:0x36
	s_barrier
	s_cbranch_scc1 .LBB0_1204
	s_add_u32 s34, s6, 0x3cf40000
	s_addc_u32 s35, s7, 0
	s_add_u32 s36, s6, 0x15540000
	s_addc_u32 s37, s7, 0
	s_ashr_i32 s39, s31, 31
	s_lshr_b32 s0, s39, 29
	s_add_i32 s0, s31, s0
	s_lshr_b32 s8, s33, 6
	s_ashr_i32 s9, s0, 3
	s_and_b32 s0, s0, -8
	s_lshr_b32 s1, s33, 8
	s_lshl_b32 s38, s8, 10
	s_sub_i32 s0, s31, s0
	s_cmp_lt_i32 s0, 0
	s_movk_i32 s40, 0x42
	s_cselect_b32 s10, s40, 0x41
	s_mul_i32 s0, s10, s0
	s_add_i32 s0, s0, s9
	s_ashr_i32 s9, s0, 31
	s_lshr_b32 s9, s9, 26
	s_add_i32 s9, s0, s9
	s_ashr_i32 s10, s9, 6
	s_lshl_b32 s12, s10, 3
	s_sub_i32 s10, 0x41, s12
	s_min_u32 s13, s10, 8
	s_andn2_b32 s9, s9, 63
	s_sub_i32 s9, s0, s9
	v_cvt_f32_ubyte0_e32 v3, s13
	v_cvt_f32_i32_e32 v2, s9
	v_rcp_iflag_f32_e32 v4, v3
	s_ashr_i32 s0, s9, 30
	s_or_b32 s0, s0, 1
	v_mov_b32_e32 v131, 0
	v_mul_f32_e32 v4, v2, v4
	v_trunc_f32_e32 v4, v4
	v_fma_f32 v2, -v4, v3, v2
	v_cvt_i32_f32_e32 v4, v4
	v_cmp_ge_f32_e64 s[10:11], |v2|, v3
	s_and_b64 s[10:11], s[10:11], exec
	s_cselect_b32 s0, s0, 0
	v_readfirstlane_b32 s10, v4
	s_add_i32 s0, s10, s0
	s_mul_i32 s10, s0, s13
	s_sub_i32 s9, s9, s10
	s_sext_i32_i8 s9, s9
	s_add_i32 s22, s12, s9
	s_ashr_i32 s23, s22, 31
	s_lshl_b64 s[10:11], s[22:23], 19
	s_add_u32 s24, s34, s10
	s_addc_u32 s25, s35, s11
	s_bfe_i64 s[10:11], s[0:1], 0x80000
	s_lshl_b64 s[10:11], s[10:11], 19
	s_add_u32 s26, s36, s10
	s_addc_u32 s27, s37, s11
	s_add_i32 s23, s38, 0
	s_add_i32 m0, s23, 0x10000
	s_add_i32 s41, s23, 0x2000
	global_load_lds_dwordx4 v130, s[26:27]
	s_add_i32 m0, s23, 0x12000
	s_add_u32 s10, s26, 0x40000
	global_load_lds_dwordx4 v132, s[26:27]
	s_mov_b32 m0, s23
	s_addc_u32 s11, s27, 0
	global_load_lds_dwordx4 v130, s[24:25]
	s_mov_b32 m0, s41
	v_mov_b32_e32 v133, v131
	global_load_lds_dwordx4 v132, s[24:25]
	s_add_i32 m0, s23, 0x14000
	s_mov_b32 s44, 0
	global_load_lds_dwordx4 v130, s[10:11]
	s_add_i32 m0, s23, 0x16000
	s_waitcnt vmcnt(0)
	v_lshl_add_u64 v[8:9], s[26:27], 0, v[130:131]
	global_load_lds_dwordx4 v132, s[10:11]
	s_add_u32 s10, s24, 0x40000
	s_addc_u32 s11, s25, 0
	s_add_i32 s42, s23, 0x4000
	s_mov_b32 m0, s42
	s_add_i32 s43, s23, 0x6000
	global_load_lds_dwordx4 v130, s[10:11]
	s_mov_b32 m0, s43
	v_lshl_add_u64 v[6:7], s[26:27], 0, v[132:133]
	global_load_lds_dwordx4 v132, s[10:11]
	v_lshl_add_u64 v[4:5], s[24:25], 0, v[130:131]
	s_cmp_lg_u32 s1, 1
	v_lshl_add_u64 v[2:3], s[24:25], 0, v[132:133]
	s_cbranch_scc1 .LBB0_1195
	s_barrier
	s_setprio 1

.LBB0_1204:
	v_cndmask_b32_e64 v2, 0, 1, s[2:3]
	v_cmp_ne_u32_e64 s[0:1], 1, v2
	s_andn2_b64 vcc, exec, s[2:3]
	v_readfirstlane_b32 s33, v0
	s_cbranch_vccnz .LBB0_1216
	s_add_u32 s34, s6, 0x4e400000
	s_addc_u32 s35, s7, 0
	s_add_u32 s36, s6, 0x15940000
	s_addc_u32 s37, s7, 0
	s_ashr_i32 s39, s31, 31
	s_lshr_b32 s2, s39, 29
	s_add_i32 s2, s31, s2
	s_lshr_b32 s8, s33, 6
	s_ashr_i32 s9, s2, 3
	s_and_b32 s2, s2, -8
	s_lshr_b32 s3, s33, 8
	s_lshl_b32 s38, s8, 10
	s_sub_i32 s2, s31, s2
	s_cmp_lt_i32 s2, 0
	s_movk_i32 s40, 0x42
	s_cselect_b32 s10, s40, 0x41
	s_mul_i32 s2, s10, s2
	s_add_i32 s2, s2, s9
	s_ashr_i32 s9, s2, 31
	s_lshr_b32 s9, s9, 26
	s_add_i32 s9, s2, s9
	s_ashr_i32 s10, s9, 6
	s_lshl_b32 s12, s10, 3
	s_sub_i32 s10, 0x41, s12
	s_min_u32 s13, s10, 8
	s_andn2_b32 s9, s9, 63
	s_sub_i32 s9, s2, s9
	v_cvt_f32_ubyte0_e32 v3, s13
	v_cvt_f32_i32_e32 v2, s9
	v_rcp_iflag_f32_e32 v4, v3
	s_ashr_i32 s2, s9, 30
	s_or_b32 s2, s2, 1
	v_mov_b32_e32 v131, 0
	v_mul_f32_e32 v4, v2, v4
	v_trunc_f32_e32 v4, v4
	v_fma_f32 v2, -v4, v3, v2
	v_cvt_i32_f32_e32 v4, v4
	v_cmp_ge_f32_e64 s[10:11], |v2|, v3
	s_and_b64 s[10:11], s[10:11], exec
	s_cselect_b32 s2, s2, 0
	v_readfirstlane_b32 s10, v4
	s_add_i32 s2, s10, s2
	s_mul_i32 s10, s2, s13
	s_sub_i32 s9, s9, s10
	s_sext_i32_i8 s9, s9
	s_add_i32 s22, s12, s9
	s_ashr_i32 s23, s22, 31
	s_lshl_b64 s[10:11], s[22:23], 19
	s_add_u32 s24, s34, s10
	s_addc_u32 s25, s35, s11
	s_bfe_i64 s[10:11], s[2:3], 0x80000
	s_lshl_b64 s[10:11], s[10:11], 19
	s_add_u32 s26, s36, s10
	s_addc_u32 s27, s37, s11
	s_add_i32 s23, s38, 0
	s_add_i32 m0, s23, 0x10000
	s_add_i32 s41, s23, 0x2000
	global_load_lds_dwordx4 v130, s[26:27]
	s_add_i32 m0, s23, 0x12000
	s_add_u32 s10, s26, 0x40000
	global_load_lds_dwordx4 v132, s[26:27]
	s_mov_b32 m0, s23
	s_addc_u32 s11, s27, 0
	global_load_lds_dwordx4 v130, s[24:25]
	s_mov_b32 m0, s41
	v_mov_b32_e32 v133, v131
	global_load_lds_dwordx4 v132, s[24:25]
	s_add_i32 m0, s23, 0x14000
	s_mov_b32 s44, 0
	global_load_lds_dwordx4 v130, s[10:11]
	s_add_i32 m0, s23, 0x16000
	s_waitcnt vmcnt(0)
	v_lshl_add_u64 v[8:9], s[26:27], 0, v[130:131]
	global_load_lds_dwordx4 v132, s[10:11]
	s_add_u32 s10, s24, 0x40000
	s_addc_u32 s11, s25, 0
	s_add_i32 s42, s23, 0x4000
	s_mov_b32 m0, s42
	s_add_i32 s43, s23, 0x6000
	global_load_lds_dwordx4 v130, s[10:11]
	s_mov_b32 m0, s43
	v_lshl_add_u64 v[6:7], s[26:27], 0, v[132:133]
	global_load_lds_dwordx4 v132, s[10:11]
	v_lshl_add_u64 v[4:5], s[24:25], 0, v[130:131]
	s_cmp_lg_u32 s3, 1
	v_lshl_add_u64 v[2:3], s[24:25], 0, v[132:133]
	s_cbranch_scc1 .LBB0_1207
	s_barrier
	s_setprio 1

.LBB0_1216:
	s_and_b64 vcc, exec, s[0:1]
	v_readfirstlane_b32 s28, v0
	s_cbranch_vccnz .LBB0_1228
	s_add_u32 s29, s6, 0x50480000
	s_addc_u32 s33, s7, 0
	s_add_u32 s34, s6, 0x15d40000
	s_addc_u32 s35, s7, 0
	s_ashr_i32 s37, s31, 31
	s_lshr_b32 s0, s37, 29
	s_add_i32 s0, s31, s0
	s_lshr_b32 s2, s28, 6
	s_ashr_i32 s3, s0, 3
	s_and_b32 s0, s0, -8
	s_lshr_b32 s1, s28, 8
	s_lshl_b32 s36, s2, 10
	s_sub_i32 s0, s31, s0
	s_cmp_lt_i32 s0, 0
	s_movk_i32 s38, 0x42
	s_cselect_b32 s8, s38, 0x41
	s_mul_i32 s0, s8, s0
	s_add_i32 s0, s0, s3
	s_ashr_i32 s3, s0, 31
	s_lshr_b32 s3, s3, 26
	s_add_i32 s3, s0, s3
	s_ashr_i32 s8, s3, 6
	s_lshl_b32 s10, s8, 3
	s_sub_i32 s8, 0x41, s10
	s_min_u32 s11, s8, 8
	s_andn2_b32 s3, s3, 63
	s_sub_i32 s3, s0, s3
	v_cvt_f32_ubyte0_e32 v3, s11
	v_cvt_f32_i32_e32 v2, s3
	v_rcp_iflag_f32_e32 v4, v3
	s_ashr_i32 s0, s3, 30
	s_or_b32 s0, s0, 1
	v_mov_b32_e32 v131, 0
	v_mul_f32_e32 v4, v2, v4
	v_trunc_f32_e32 v4, v4
	v_fma_f32 v2, -v4, v3, v2
	v_cvt_i32_f32_e32 v4, v4
	v_cmp_ge_f32_e64 s[8:9], |v2|, v3
	s_and_b64 s[8:9], s[8:9], exec
	s_cselect_b32 s0, s0, 0
	v_readfirstlane_b32 s8, v4
	s_add_i32 s0, s8, s0
	s_mul_i32 s8, s0, s11
	s_sub_i32 s3, s3, s8
	s_sext_i32_i8 s3, s3
	s_add_i32 s20, s10, s3
	s_ashr_i32 s21, s20, 31
	s_lshl_b64 s[8:9], s[20:21], 19
	s_add_u32 s22, s29, s8
	s_addc_u32 s23, s33, s9
	s_bfe_i64 s[8:9], s[0:1], 0x80000
	s_lshl_b64 s[8:9], s[8:9], 19
	s_add_u32 s24, s34, s8
	s_addc_u32 s25, s35, s9
	s_add_i32 s21, s36, 0
	s_add_i32 m0, s21, 0x10000
	s_add_i32 s39, s21, 0x2000
	global_load_lds_dwordx4 v130, s[24:25]
	s_add_i32 m0, s21, 0x12000
	s_add_u32 s8, s24, 0x40000
	global_load_lds_dwordx4 v132, s[24:25]
	s_mov_b32 m0, s21
	s_addc_u32 s9, s25, 0
	global_load_lds_dwordx4 v130, s[22:23]
	s_mov_b32 m0, s39
	v_mov_b32_e32 v133, v131
	global_load_lds_dwordx4 v132, s[22:23]
	s_add_i32 m0, s21, 0x14000
	s_mov_b32 s42, 0
	global_load_lds_dwordx4 v130, s[8:9]
	s_add_i32 m0, s21, 0x16000
	s_waitcnt vmcnt(0)
	v_lshl_add_u64 v[8:9], s[24:25], 0, v[130:131]
	global_load_lds_dwordx4 v132, s[8:9]
	s_add_u32 s8, s22, 0x40000
	s_addc_u32 s9, s23, 0
	s_add_i32 s40, s21, 0x4000
	s_mov_b32 m0, s40
	s_add_i32 s41, s21, 0x6000
	global_load_lds_dwordx4 v130, s[8:9]
	s_mov_b32 m0, s41
	v_lshl_add_u64 v[6:7], s[24:25], 0, v[132:133]
	global_load_lds_dwordx4 v132, s[8:9]
	v_lshl_add_u64 v[4:5], s[22:23], 0, v[130:131]
	s_cmp_lg_u32 s1, 1
	v_lshl_add_u64 v[2:3], s[22:23], 0, v[132:133]
	s_cbranch_scc1 .LBB0_1219
	s_barrier
	s_setprio 1

.LBB0_1279:
	s_cmp_lt_i32 s54, 8
	s_cselect_b64 s[2:3], -1, 0
	s_and_b64 s[0:1], s[2:3], s[0:1]
	s_andn2_b64 vcc, exec, s[0:1]
	s_cbranch_vccnz .LBB0_1293
	v_mov_b32_e32 v1, v248
	s_waitcnt vmcnt(11)
	v_mov_b32_e32 v2, v0
	v_readlane_b32 s28, v250, 1
	v_readlane_b32 s29, v250, 0
	v_readlane_b32 s0, v250, 39
	s_mov_b64 s[0:1], s[90:91]
	s_mov_b64 s[4:5], s[52:53]
	s_cmpk_gt_i32 s29, 0x207
	v_readfirstlane_b32 s30, v0
	s_barrier
	s_cbranch_scc1 .LBB0_1292
	s_add_u32 s31, s4, 0x2ab40000
	s_addc_u32 s33, s5, 0
	v_lshlrev_b32_e32 v1, 4, v0
	s_add_u32 s34, s4, 0x16140000
	s_waitcnt vmcnt(9)
	v_or_b32_e32 v10, 0x2000, v1
	s_addc_u32 s35, s5, 0
	v_lshrrev_b32_e32 v2, 7, v10
	v_bfe_u32 v13, v0, 2, 4
	s_movk_i32 s0, 0x70
	s_ashr_i32 s37, s29, 31
	v_and_or_b32 v2, v2, s0, v13
	s_lshr_b32 s0, s37, 29
	s_add_i32 s0, s29, s0
	s_ashr_i32 s7, s0, 3
	s_and_b32 s0, s0, -8
	s_sub_i32 s0, s29, s0
	s_lshr_b32 s8, s0, 31
	s_addk_i32 s8, 0x41
	s_mul_i32 s0, s8, s0
	s_add_i32 s0, s0, s7
	s_ashr_i32 s7, s0, 31
	s_lshr_b32 s7, s7, 26
	s_add_i32 s7, s0, s7
	s_ashr_i32 s8, s7, 6
	s_lshl_b32 s10, s8, 3
	s_sub_i32 s8, 0x41, s10
	s_min_u32 s11, s8, 8
	s_andn2_b32 s7, s7, 63
	v_and_b32_e32 v3, 32, v0
	s_sub_i32 s7, s0, s7
	v_cvt_f32_ubyte0_e32 v4, s11
	v_bitop3_b32 v11, v1, v3, 48 bitop3:0x6c
	v_and_b32_e32 v12, 64, v0
	v_cvt_f32_i32_e32 v3, s7
	v_rcp_iflag_f32_e32 v5, v4
	v_or_b32_e32 v1, v11, v12
	v_lshl_or_b32 v130, v2, 12, v1
	v_lshrrev_b32_e32 v2, 3, v0
	v_and_or_b32 v2, v2, 48, v13
	v_lshl_or_b32 v132, v2, 12, v1
	v_mul_f32_e32 v1, v3, v5
	v_trunc_f32_e32 v1, v1
	v_fma_f32 v2, -v1, v4, v3
	v_cvt_i32_f32_e32 v1, v1
	s_lshr_b32 s6, s30, 6
	s_ashr_i32 s0, s7, 30
	s_lshr_b32 s1, s30, 8
	s_lshl_b32 s36, s6, 10
	s_or_b32 s0, s0, 1
	v_cmp_ge_f32_e64 s[8:9], |v2|, v4
	s_and_b64 s[8:9], s[8:9], exec
	s_cselect_b32 s0, s0, 0
	v_readfirstlane_b32 s8, v1
	s_add_i32 s0, s8, s0
	s_mul_i32 s8, s0, s11
	s_sub_i32 s7, s7, s8
	s_sext_i32_i8 s7, s7
	s_add_i32 s20, s10, s7
	s_ashr_i32 s21, s20, 31
	s_lshl_b64 s[8:9], s[20:21], 20
	s_add_u32 s22, s31, s8
	s_addc_u32 s23, s33, s9
	s_bfe_i64 s[8:9], s[0:1], 0x80000
	s_lshl_b64 s[8:9], s[8:9], 20
	s_add_u32 s24, s34, s8
	s_addc_u32 s25, s35, s9
	s_add_i32 s21, s36, 0
	s_add_i32 m0, s21, 0x10000
	s_add_i32 s38, s21, 0x2000
	global_load_lds_dwordx4 v132, s[24:25]
	s_add_i32 m0, s21, 0x12000
	s_add_u32 s8, s24, 0x80000
	global_load_lds_dwordx4 v130, s[24:25]
	s_mov_b32 m0, s21
	s_addc_u32 s9, s25, 0
	global_load_lds_dwordx4 v132, s[22:23]
	s_mov_b32 m0, s38
	v_mov_b32_e32 v135, 0
	global_load_lds_dwordx4 v130, s[22:23]
	s_add_i32 m0, s21, 0x14000
	v_mov_b32_e32 v133, v135
	global_load_lds_dwordx4 v132, s[8:9]
	s_add_i32 m0, s21, 0x16000
	v_mov_b32_e32 v131, v135
	global_load_lds_dwordx4 v130, s[8:9]
	s_add_u32 s8, s22, 0x80000
	s_addc_u32 s9, s23, 0
	s_add_i32 s39, s21, 0x4000
	s_mov_b32 m0, s39
	s_add_i32 s40, s21, 0x6000
	global_load_lds_dwordx4 v132, s[8:9]
	s_mov_b32 m0, s40
	s_mov_b32 s41, 0
	global_load_lds_dwordx4 v130, s[8:9]
	v_lshl_add_u64 v[8:9], s[24:25], 0, v[132:133]
	v_lshl_add_u64 v[6:7], s[24:25], 0, v[130:131]
	v_lshl_add_u64 v[4:5], s[22:23], 0, v[132:133]
	s_cmp_lg_u32 s1, 1
	v_lshl_add_u64 v[2:3], s[22:23], 0, v[130:131]
	v_readlane_b32 s44, v250, 7
	v_readlane_b32 s45, v250, 8
	v_readlane_b32 s46, v250, 9
	v_readlane_b32 s47, v250, 10
	v_readlane_b32 s48, v250, 11
	v_readlane_b32 s49, v250, 12
	v_readlane_b32 s50, v250, 13
	v_readlane_b32 s51, v250, 14
	v_readlane_b32 s52, v250, 15
	v_readlane_b32 s53, v250, 16
	v_readlane_b32 s54, v250, 17
	v_readlane_b32 s55, v250, 18
	v_readlane_b32 s56, v250, 19
	v_readlane_b32 s57, v250, 20
	v_readlane_b32 s58, v250, 21
	v_readlane_b32 s59, v250, 22
	s_cbranch_scc1 .LBB0_1283
	s_barrier
	s_setprio 1

.LBB0_1287:
	ds_read_b128 v[144:147], v150
	ds_read_b128 v[154:157], v150 offset:1024
	ds_read_b128 v[158:161], v150 offset:2048
	ds_read_b128 v[162:165], v150 offset:3072
	s_add_u32 s24, s22, 0xfff80080
	s_addc_u32 s25, s23, -1
	s_cmp_eq_u32 s53, 28
	s_cselect_b32 s27, s15, s25
	s_cselect_b32 s26, s49, s24
	s_cselect_b32 s25, s13, s52
	s_cselect_b32 s24, s50, s51
	v_lshl_add_u64 v[190:191], s[22:23], 0, v[136:137]
	s_add_i32 m0, s21, 0xc000
	ds_read_b128 v[166:169], v151
	ds_read_b128 v[170:173], v151 offset:1024
	ds_read_b128 v[174:177], v151 offset:2048
	ds_read_b128 v[178:181], v151 offset:3072
	ds_read_b128 v[182:185], v151 offset:4096
	ds_read_b128 v[186:189], v151 offset:5120
	ds_read_b128 v[192:195], v151 offset:6144
	ds_read_b128 v[196:199], v151 offset:7168
	global_load_lds_dwordx4 v[190:191], off
	v_lshl_add_u64 v[190:191], s[22:23], 0, v[138:139]
	s_add_i32 m0, s21, 0xe000
	s_nop 0
	global_load_lds_dwordx4 v[190:191], off
	s_waitcnt lgkmcnt(8)
	s_barrier
	s_waitcnt lgkmcnt(0)
	s_waitcnt lgkmcnt(0)
	v_mfma_f32_16x16x32_bf16 v[126:129], v[144:147], v[166:169], v[126:129]
	v_mfma_f32_16x16x32_bf16 v[122:125], v[158:161], v[166:169], v[122:125]
	v_mfma_f32_16x16x32_bf16 v[114:117], v[144:147], v[174:177], v[114:117]
	v_mfma_f32_16x16x32_bf16 v[106:109], v[158:161], v[174:177], v[106:109]
	v_mfma_f32_16x16x32_bf16 v[98:101], v[144:147], v[182:185], v[98:101]
	v_mfma_f32_16x16x32_bf16 v[90:93], v[158:161], v[182:185], v[90:93]
	v_mfma_f32_16x16x32_bf16 v[82:85], v[144:147], v[192:195], v[82:85]
	v_mfma_f32_16x16x32_bf16 v[74:77], v[158:161], v[192:195], v[74:77]
	v_mfma_f32_16x16x32_bf16 v[126:129], v[154:157], v[170:173], v[126:129]
	v_mfma_f32_16x16x32_bf16 v[122:125], v[162:165], v[170:173], v[122:125]
	v_mfma_f32_16x16x32_bf16 v[114:117], v[154:157], v[178:181], v[114:117]
	v_mfma_f32_16x16x32_bf16 v[106:109], v[162:165], v[178:181], v[106:109]
	v_mfma_f32_16x16x32_bf16 v[98:101], v[154:157], v[186:189], v[98:101]
	v_mfma_f32_16x16x32_bf16 v[90:93], v[162:165], v[186:189], v[90:93]
	v_mfma_f32_16x16x32_bf16 v[82:85], v[154:157], v[196:199], v[82:85]
	v_mfma_f32_16x16x32_bf16 v[74:77], v[162:165], v[196:199], v[74:77]
	s_barrier
	s_add_i32 s54, s45, s36
	v_lshl_add_u64 v[190:191], s[24:25], 0, v[132:133]
	s_mov_b32 m0, s54
	ds_read_b128 v[200:203], v152
	ds_read_b128 v[204:207], v152 offset:1024
	ds_read_b128 v[208:211], v152 offset:2048
	ds_read_b128 v[212:215], v152 offset:3072
	global_load_lds_dwordx4 v[190:191], off
	v_lshl_add_u64 v[216:217], s[24:25], 0, v[130:131]
	s_add_i32 m0, s54, 0x2000
	s_nop 0
	global_load_lds_dwordx4 v[216:217], off
	s_barrier
	s_waitcnt lgkmcnt(0)
	s_waitcnt lgkmcnt(0)
	v_mfma_f32_16x16x32_bf16 v[118:121], v[200:203], v[166:169], v[118:121]
	v_mfma_f32_16x16x32_bf16 v[110:113], v[208:211], v[166:169], v[110:113]
	v_mfma_f32_16x16x32_bf16 v[102:105], v[200:203], v[174:177], v[102:105]
	v_mfma_f32_16x16x32_bf16 v[94:97], v[208:211], v[174:177], v[94:97]
	v_mfma_f32_16x16x32_bf16 v[86:89], v[200:203], v[182:185], v[86:89]
	v_mfma_f32_16x16x32_bf16 v[78:81], v[208:211], v[182:185], v[78:81]
	v_mfma_f32_16x16x32_bf16 v[70:73], v[200:203], v[192:195], v[70:73]
	v_mfma_f32_16x16x32_bf16 v[66:69], v[208:211], v[192:195], v[66:69]
	v_mfma_f32_16x16x32_bf16 v[118:121], v[204:207], v[170:173], v[118:121]
	v_mfma_f32_16x16x32_bf16 v[110:113], v[212:215], v[170:173], v[110:113]
	v_mfma_f32_16x16x32_bf16 v[102:105], v[204:207], v[178:181], v[102:105]
	v_mfma_f32_16x16x32_bf16 v[94:97], v[212:215], v[178:181], v[94:97]
	v_mfma_f32_16x16x32_bf16 v[86:89], v[204:207], v[186:189], v[86:89]
	v_mfma_f32_16x16x32_bf16 v[78:81], v[212:215], v[186:189], v[78:81]
	v_mfma_f32_16x16x32_bf16 v[70:73], v[204:207], v[196:199], v[70:73]
	v_mfma_f32_16x16x32_bf16 v[66:69], v[212:215], v[196:199], v[66:69]
	s_mov_b32 m0, s21
	v_lshl_add_u64 v[218:219], s[26:27], 0, v[132:133]
	s_barrier
	ds_read_b128 v[166:169], v151 offset:16384
	ds_read_b128 v[170:173], v151 offset:17408
	ds_read_b128 v[174:177], v151 offset:18432
	ds_read_b128 v[178:181], v151 offset:19456
	ds_read_b128 v[182:185], v151 offset:20480
	ds_read_b128 v[186:189], v151 offset:21504
	ds_read_b128 v[192:195], v151 offset:22528
	ds_read_b128 v[196:199], v151 offset:23552
	global_load_lds_dwordx4 v[218:219], off
	v_lshl_add_u64 v[220:221], s[26:27], 0, v[130:131]
	s_mov_b32 m0, s38
	s_nop 0
	global_load_lds_dwordx4 v[220:221], off
	s_barrier
	s_waitcnt lgkmcnt(0)
	s_waitcnt lgkmcnt(0)
	v_mfma_f32_16x16x32_bf16 v[62:65], v[144:147], v[166:169], v[62:65]
	v_mfma_f32_16x16x32_bf16 v[58:61], v[158:161], v[166:169], v[58:61]
	v_mfma_f32_16x16x32_bf16 v[50:53], v[144:147], v[174:177], v[50:53]
	v_mfma_f32_16x16x32_bf16 v[42:45], v[158:161], v[174:177], v[42:45]
	v_mfma_f32_16x16x32_bf16 v[34:37], v[144:147], v[182:185], v[34:37]
	v_mfma_f32_16x16x32_bf16 v[26:29], v[158:161], v[182:185], v[26:29]
	v_mfma_f32_16x16x32_bf16 v[18:21], v[144:147], v[192:195], v[18:21]
	v_mfma_f32_16x16x32_bf16 v[10:13], v[158:161], v[192:195], v[10:13]
	v_mfma_f32_16x16x32_bf16 v[62:65], v[154:157], v[170:173], v[62:65]
	v_mfma_f32_16x16x32_bf16 v[58:61], v[162:165], v[170:173], v[58:61]
	v_mfma_f32_16x16x32_bf16 v[50:53], v[154:157], v[178:181], v[50:53]
	v_mfma_f32_16x16x32_bf16 v[42:45], v[162:165], v[178:181], v[42:45]
	v_mfma_f32_16x16x32_bf16 v[34:37], v[154:157], v[186:189], v[34:37]
	v_mfma_f32_16x16x32_bf16 v[26:29], v[162:165], v[186:189], v[26:29]
	v_mfma_f32_16x16x32_bf16 v[18:21], v[154:157], v[196:199], v[18:21]
	v_mfma_f32_16x16x32_bf16 v[10:13], v[162:165], v[196:199], v[10:13]
	s_barrier
	s_add_u32 s54, s24, 0x80000
	s_addc_u32 s55, s25, 0
	s_add_i32 s56, s46, s36
	v_lshl_add_u64 v[144:145], s[54:55], 0, v[132:133]
	s_mov_b32 m0, s56
	s_nop 0
	global_load_lds_dwordx4 v[144:145], off
	v_lshl_add_u64 v[144:145], s[54:55], 0, v[130:131]
	s_add_i32 m0, s56, 0x2000
	s_nop 0
	global_load_lds_dwordx4 v[144:145], off
	s_waitcnt vmcnt(6)
	s_barrier
	v_mfma_f32_16x16x32_bf16 v[54:57], v[200:203], v[166:169], v[54:57]
	v_mfma_f32_16x16x32_bf16 v[46:49], v[208:211], v[166:169], v[46:49]
	v_mfma_f32_16x16x32_bf16 v[38:41], v[200:203], v[174:177], v[38:41]
	v_mfma_f32_16x16x32_bf16 v[30:33], v[208:211], v[174:177], v[30:33]
	v_mfma_f32_16x16x32_bf16 v[22:25], v[200:203], v[182:185], v[22:25]
	v_mfma_f32_16x16x32_bf16 v[14:17], v[208:211], v[182:185], v[14:17]
	v_mfma_f32_16x16x32_bf16 v[6:9], v[200:203], v[192:195], v[6:9]
	v_mfma_f32_16x16x32_bf16 v[2:5], v[208:211], v[192:195], v[2:5]
	v_mfma_f32_16x16x32_bf16 v[54:57], v[204:207], v[170:173], v[54:57]
	v_mfma_f32_16x16x32_bf16 v[46:49], v[212:215], v[170:173], v[46:49]
	v_mfma_f32_16x16x32_bf16 v[38:41], v[204:207], v[178:181], v[38:41]
	v_mfma_f32_16x16x32_bf16 v[30:33], v[212:215], v[178:181], v[30:33]
	v_mfma_f32_16x16x32_bf16 v[22:25], v[204:207], v[186:189], v[22:25]
	v_mfma_f32_16x16x32_bf16 v[14:17], v[212:215], v[186:189], v[14:17]
	v_mfma_f32_16x16x32_bf16 v[6:9], v[204:207], v[196:199], v[6:9]
	v_mfma_f32_16x16x32_bf16 v[2:5], v[212:215], v[196:199], v[2:5]
	s_add_i32 s54, 0, 0x18000
	v_add_u32_e32 v134, s54, v148
	s_barrier
	ds_read_b128 v[144:147], v134
	ds_read_b128 v[154:157], v134 offset:1024
	ds_read_b128 v[158:161], v134 offset:2048
	ds_read_b128 v[162:165], v134 offset:3072
	s_add_u32 s26, s26, 0x80000
	s_addc_u32 s27, s27, 0
	s_mov_b32 m0, s39
	v_lshl_add_u64 v[200:201], s[26:27], 0, v[132:133]
	ds_read_b128 v[166:169], v151 offset:32768
	ds_read_b128 v[170:173], v151 offset:33792
	ds_read_b128 v[174:177], v151 offset:34816
	ds_read_b128 v[178:181], v151 offset:35840
	ds_read_b128 v[182:185], v151 offset:36864
	ds_read_b128 v[186:189], v151 offset:37888
	ds_read_b128 v[192:195], v151 offset:38912
	ds_read_b128 v[196:199], v151 offset:39936
	global_load_lds_dwordx4 v[200:201], off
	v_lshl_add_u64 v[200:201], s[26:27], 0, v[130:131]
	s_mov_b32 m0, s40
	s_nop 0
	global_load_lds_dwordx4 v[200:201], off
	s_waitcnt lgkmcnt(8)
	s_barrier
	s_waitcnt lgkmcnt(0)
	s_waitcnt lgkmcnt(0)
	v_mfma_f32_16x16x32_bf16 v[126:129], v[144:147], v[166:169], v[126:129]
	v_mfma_f32_16x16x32_bf16 v[122:125], v[158:161], v[166:169], v[122:125]
	v_mfma_f32_16x16x32_bf16 v[114:117], v[144:147], v[174:177], v[114:117]
	v_mfma_f32_16x16x32_bf16 v[106:109], v[158:161], v[174:177], v[106:109]
	v_mfma_f32_16x16x32_bf16 v[98:101], v[144:147], v[182:185], v[98:101]
	v_mfma_f32_16x16x32_bf16 v[90:93], v[158:161], v[182:185], v[90:93]
	v_mfma_f32_16x16x32_bf16 v[82:85], v[144:147], v[192:195], v[82:85]
	v_mfma_f32_16x16x32_bf16 v[74:77], v[158:161], v[192:195], v[74:77]
	v_mfma_f32_16x16x32_bf16 v[126:129], v[154:157], v[170:173], v[126:129]
	v_mfma_f32_16x16x32_bf16 v[122:125], v[162:165], v[170:173], v[122:125]
	v_mfma_f32_16x16x32_bf16 v[114:117], v[154:157], v[178:181], v[114:117]
	v_mfma_f32_16x16x32_bf16 v[106:109], v[162:165], v[178:181], v[106:109]
	v_mfma_f32_16x16x32_bf16 v[98:101], v[154:157], v[186:189], v[98:101]
	v_mfma_f32_16x16x32_bf16 v[90:93], v[162:165], v[186:189], v[90:93]
	v_mfma_f32_16x16x32_bf16 v[82:85], v[154:157], v[196:199], v[82:85]
	v_mfma_f32_16x16x32_bf16 v[74:77], v[162:165], v[196:199], v[74:77]
	s_barrier
	s_add_i32 s26, 0, 0x1c000
	s_add_i32 s27, s54, s36
	v_add_u32_e32 v134, s26, v148
	v_lshl_add_u64 v[190:191], v[190:191], 0, s[6:7]
	s_mov_b32 m0, s27
	ds_read_b128 v[200:203], v134
	ds_read_b128 v[204:207], v134 offset:1024
	ds_read_b128 v[208:211], v134 offset:2048
	ds_read_b128 v[212:215], v134 offset:3072
	global_load_lds_dwordx4 v[190:191], off
	v_lshl_add_u64 v[190:191], v[216:217], 0, s[6:7]
	s_add_i32 m0, s27, 0x2000
	s_nop 0
	global_load_lds_dwordx4 v[190:191], off
	s_barrier
	s_waitcnt lgkmcnt(0)
	s_waitcnt lgkmcnt(0)
	v_mfma_f32_16x16x32_bf16 v[118:121], v[200:203], v[166:169], v[118:121]
	v_mfma_f32_16x16x32_bf16 v[110:113], v[208:211], v[166:169], v[110:113]
	v_mfma_f32_16x16x32_bf16 v[102:105], v[200:203], v[174:177], v[102:105]
	v_mfma_f32_16x16x32_bf16 v[94:97], v[208:211], v[174:177], v[94:97]
	v_mfma_f32_16x16x32_bf16 v[86:89], v[200:203], v[182:185], v[86:89]
	v_mfma_f32_16x16x32_bf16 v[78:81], v[208:211], v[182:185], v[78:81]
	v_mfma_f32_16x16x32_bf16 v[70:73], v[200:203], v[192:195], v[70:73]
	v_mfma_f32_16x16x32_bf16 v[66:69], v[208:211], v[192:195], v[66:69]
	v_mfma_f32_16x16x32_bf16 v[118:121], v[204:207], v[170:173], v[118:121]
	v_mfma_f32_16x16x32_bf16 v[110:113], v[212:215], v[170:173], v[110:113]
	v_mfma_f32_16x16x32_bf16 v[102:105], v[204:207], v[178:181], v[102:105]
	v_mfma_f32_16x16x32_bf16 v[94:97], v[212:215], v[178:181], v[94:97]
	v_mfma_f32_16x16x32_bf16 v[86:89], v[204:207], v[186:189], v[86:89]
	v_mfma_f32_16x16x32_bf16 v[78:81], v[212:215], v[186:189], v[78:81]
	v_mfma_f32_16x16x32_bf16 v[70:73], v[204:207], v[196:199], v[70:73]
	v_mfma_f32_16x16x32_bf16 v[66:69], v[212:215], v[196:199], v[66:69]
	s_mov_b32 m0, s42
	v_lshl_add_u64 v[190:191], v[218:219], 0, s[6:7]
	s_barrier
	ds_read_b128 v[166:169], v151 offset:49152
	ds_read_b128 v[170:173], v151 offset:50176
	ds_read_b128 v[174:177], v151 offset:51200
	ds_read_b128 v[178:181], v151 offset:52224
	ds_read_b128 v[182:185], v151 offset:53248
	ds_read_b128 v[186:189], v151 offset:54272
	ds_read_b128 v[192:195], v151 offset:55296
	ds_read_b128 v[196:199], v151 offset:56320
	global_load_lds_dwordx4 v[190:191], off
	v_lshl_add_u64 v[190:191], v[220:221], 0, s[6:7]
	s_mov_b32 m0, s43
	s_nop 0
	global_load_lds_dwordx4 v[190:191], off
	s_barrier
	s_waitcnt lgkmcnt(0)
	s_waitcnt lgkmcnt(0)
	v_mfma_f32_16x16x32_bf16 v[62:65], v[144:147], v[166:169], v[62:65]
	v_mfma_f32_16x16x32_bf16 v[58:61], v[158:161], v[166:169], v[58:61]
	v_mfma_f32_16x16x32_bf16 v[50:53], v[144:147], v[174:177], v[50:53]
	v_mfma_f32_16x16x32_bf16 v[42:45], v[158:161], v[174:177], v[42:45]
	v_mfma_f32_16x16x32_bf16 v[34:37], v[144:147], v[182:185], v[34:37]
	v_mfma_f32_16x16x32_bf16 v[26:29], v[158:161], v[182:185], v[26:29]
	v_mfma_f32_16x16x32_bf16 v[18:21], v[144:147], v[192:195], v[18:21]
	v_mfma_f32_16x16x32_bf16 v[10:13], v[158:161], v[192:195], v[10:13]
	v_mfma_f32_16x16x32_bf16 v[62:65], v[154:157], v[170:173], v[62:65]
	v_mfma_f32_16x16x32_bf16 v[58:61], v[162:165], v[170:173], v[58:61]
	v_mfma_f32_16x16x32_bf16 v[50:53], v[154:157], v[178:181], v[50:53]
	v_mfma_f32_16x16x32_bf16 v[42:45], v[162:165], v[178:181], v[42:45]
	v_mfma_f32_16x16x32_bf16 v[34:37], v[154:157], v[186:189], v[34:37]
	v_mfma_f32_16x16x32_bf16 v[26:29], v[162:165], v[186:189], v[26:29]
	v_mfma_f32_16x16x32_bf16 v[18:21], v[154:157], v[196:199], v[18:21]
	v_mfma_f32_16x16x32_bf16 v[10:13], v[162:165], v[196:199], v[10:13]
	s_barrier
	s_add_u32 s24, s24, 0x80080
	s_addc_u32 s25, s25, 0
	s_add_i32 s26, s26, s36
	v_lshl_add_u64 v[144:145], s[24:25], 0, v[132:133]
	s_mov_b32 m0, s26
	s_nop 0
	global_load_lds_dwordx4 v[144:145], off
	v_lshl_add_u64 v[144:145], s[24:25], 0, v[130:131]
	s_add_i32 m0, s26, 0x2000
	s_nop 0
	global_load_lds_dwordx4 v[144:145], off
	s_waitcnt vmcnt(6)
	s_barrier
	v_mfma_f32_16x16x32_bf16 v[54:57], v[200:203], v[166:169], v[54:57]
	v_mfma_f32_16x16x32_bf16 v[46:49], v[208:211], v[166:169], v[46:49]
	v_mfma_f32_16x16x32_bf16 v[38:41], v[200:203], v[174:177], v[38:41]
	v_mfma_f32_16x16x32_bf16 v[30:33], v[208:211], v[174:177], v[30:33]
	v_mfma_f32_16x16x32_bf16 v[22:25], v[200:203], v[182:185], v[22:25]
	v_mfma_f32_16x16x32_bf16 v[14:17], v[208:211], v[182:185], v[14:17]
	v_mfma_f32_16x16x32_bf16 v[6:9], v[200:203], v[192:195], v[6:9]
	v_mfma_f32_16x16x32_bf16 v[2:5], v[208:211], v[192:195], v[2:5]
	v_mfma_f32_16x16x32_bf16 v[54:57], v[204:207], v[170:173], v[54:57]
	v_mfma_f32_16x16x32_bf16 v[46:49], v[212:215], v[170:173], v[46:49]
	v_mfma_f32_16x16x32_bf16 v[38:41], v[204:207], v[178:181], v[38:41]
	v_mfma_f32_16x16x32_bf16 v[30:33], v[212:215], v[178:181], v[30:33]
	v_mfma_f32_16x16x32_bf16 v[22:25], v[204:207], v[186:189], v[22:25]
	v_mfma_f32_16x16x32_bf16 v[14:17], v[212:215], v[186:189], v[14:17]
	v_mfma_f32_16x16x32_bf16 v[6:9], v[204:207], v[196:199], v[6:9]
	v_mfma_f32_16x16x32_bf16 v[2:5], v[212:215], v[196:199], v[2:5]
	s_add_i32 s53, s53, 2
	s_add_u32 s22, s22, 0x100
	s_addc_u32 s23, s23, 0
	s_add_u32 s51, s51, 0x100
	s_addc_u32 s52, s52, 0
	s_cmp_gt_u32 s53, 29
	s_barrier
	s_cbranch_scc0 .LBB0_1287
	v_lshl_add_u32 v144, s20, 8, v1
	s_movk_i32 s13, 0x4000
	v_lshl_or_b32 v146, s48, 8, v149
	v_ashrrev_i32_e32 v134, 31, v144
	v_cmp_gt_i32_e32 vcc, s13, v144
	v_readlane_b32 s48, v250, 7
	v_add_u32_e32 v154, 0xffffc000, v144
	v_cndmask_b32_e32 v145, 0, v134, vcc
	v_readlane_b32 s49, v250, 8
	v_readlane_b32 s52, v250, 11
	v_readlane_b32 s53, v250, 12
	v_cndmask_b32_e32 v158, v154, v144, vcc
	v_mov_b32_e32 v159, v145
	v_mov_b32_e32 v154, s53
	v_mov_b32_e32 v155, s49
	v_mov_b32_e32 v156, s52
	v_mov_b32_e32 v157, s48
	s_movk_i32 s13, 0x3fff
	v_ashrrev_i32_e32 v147, 31, v146
	v_cndmask_b32_e32 v161, v154, v155, vcc
	v_cndmask_b32_e32 v160, v156, v157, vcc
	v_lshlrev_b64 v[158:159], 13, v[158:159]
	v_cmp_lt_i32_e32 vcc, s13, v144
	v_lshl_add_u64 v[158:159], v[160:161], 0, v[158:159]
	v_lshlrev_b64 v[146:147], 2, v[146:147]
	v_cndmask_b32_e32 v134, 0, v153, vcc
	v_lshl_add_u64 v[166:167], v[158:159], 0, v[146:147]
	v_lshl_add_u64 v[158:159], s[4:5], 0, v[134:135]
	v_lshl_add_u64 v[168:169], v[158:159], 0, v[146:147]
	v_add_co_u32_e32 v158, vcc, s47, v168
	v_lshlrev_b64 v[170:171], 13, v[144:145]
	s_nop 0
	v_addc_co_u32_e32 v159, vcc, 0, v169, vcc
	v_lshl_add_u64 v[170:171], s[8:9], 0, v[170:171]
	v_lshl_add_u64 v[170:171], v[170:171], 0, v[146:147]
	v_lshl_add_u64 v[168:169], v[168:169], 0, s[10:11]
	global_load_dwordx4 v[144:147], v[158:159], off
	global_load_dwordx4 v[154:157], v[168:169], off offset:64
	global_load_dwordx4 v[160:163], v[168:169], off offset:512
	global_load_dwordx4 v[172:175], v[168:169], off offset:576
	global_load_dwordx4 v[176:179], v[166:167], off
	global_load_dwordx4 v[180:183], v[166:167], off offset:64
	global_load_dwordx4 v[184:187], v[166:167], off offset:512
	global_load_dwordx4 v[192:195], v[166:167], off offset:576
	v_add_co_u32_e32 v188, vcc, 0x20000, v166
	s_nop 1
	v_addc_co_u32_e32 v189, vcc, 0, v167, vcc
	global_load_dwordx4 v[196:199], v[188:189], off
	global_load_dwordx4 v[200:203], v[188:189], off offset:64
	global_load_dwordx4 v[204:207], v[188:189], off offset:512
	global_load_dwordx4 v[208:211], v[188:189], off offset:576
	v_add_co_u32_e32 v214, vcc, 0x20000, v170
	s_nop 1
	v_addc_co_u32_e32 v215, vcc, 0, v171, vcc
	s_waitcnt vmcnt(7)
	v_pk_fma_f32 v[128:129], v[128:129], v[146:147], v[178:179]
	v_pk_fma_f32 v[126:127], v[126:127], v[144:145], v[176:177]
	global_store_dwordx4 v[170:171], v[126:129], off
	s_waitcnt vmcnt(7)
	v_pk_fma_f32 v[124:125], v[124:125], v[156:157], v[182:183]
	v_pk_fma_f32 v[122:123], v[122:123], v[154:155], v[180:181]
	global_store_dwordx4 v[170:171], v[122:125], off offset:64
	s_waitcnt vmcnt(7)
	v_pk_fma_f32 v[120:121], v[120:121], v[162:163], v[186:187]
	v_pk_fma_f32 v[118:119], v[118:119], v[160:161], v[184:185]
	global_store_dwordx4 v[170:171], v[118:121], off offset:512
	s_waitcnt vmcnt(7)
	v_pk_fma_f32 v[112:113], v[112:113], v[174:175], v[194:195]
	v_pk_fma_f32 v[110:111], v[110:111], v[172:173], v[192:193]
	global_store_dwordx4 v[170:171], v[110:113], off offset:576
	s_waitcnt vmcnt(7)
	v_pk_fma_f32 v[116:117], v[116:117], v[146:147], v[198:199]
	v_pk_fma_f32 v[114:115], v[114:115], v[144:145], v[196:197]
	global_store_dwordx4 v[214:215], v[114:117], off
	s_waitcnt vmcnt(7)
	v_pk_fma_f32 v[108:109], v[108:109], v[156:157], v[202:203]
	v_pk_fma_f32 v[106:107], v[106:107], v[154:155], v[200:201]
	global_store_dwordx4 v[214:215], v[106:109], off offset:64
	s_waitcnt vmcnt(7)
	v_pk_fma_f32 v[104:105], v[104:105], v[162:163], v[206:207]
	v_pk_fma_f32 v[102:103], v[102:103], v[160:161], v[204:205]
	global_store_dwordx4 v[214:215], v[102:105], off offset:512
	s_waitcnt vmcnt(7)
	v_pk_fma_f32 v[96:97], v[96:97], v[174:175], v[210:211]
	v_pk_fma_f32 v[94:95], v[94:95], v[172:173], v[208:209]
	global_store_dwordx4 v[214:215], v[94:97], off offset:576
	v_add_co_u32_e32 v164, vcc, 0x40000, v166
	s_nop 1
	v_addc_co_u32_e32 v165, vcc, 0, v167, vcc
	global_load_dwordx4 v[176:179], v[164:165], off
	global_load_dwordx4 v[180:183], v[164:165], off offset:64
	global_load_dwordx4 v[184:187], v[164:165], off offset:512
	global_load_dwordx4 v[192:195], v[164:165], off offset:576
	v_add_co_u32_e32 v188, vcc, 0x60000, v166
	s_nop 1
	v_addc_co_u32_e32 v189, vcc, 0, v167, vcc
	global_load_dwordx4 v[196:199], v[188:189], off
	global_load_dwordx4 v[200:203], v[188:189], off offset:64
	global_load_dwordx4 v[204:207], v[188:189], off offset:512
	global_load_dwordx4 v[208:211], v[188:189], off offset:576
	v_add_co_u32_e32 v212, vcc, 0x40000, v170
	s_nop 1
	v_addc_co_u32_e32 v213, vcc, 0, v171, vcc
	v_add_co_u32_e32 v214, vcc, 0x60000, v170
	s_nop 1
	v_addc_co_u32_e32 v215, vcc, 0, v171, vcc
	s_waitcnt vmcnt(7)
	v_pk_fma_f32 v[100:101], v[100:101], v[146:147], v[178:179]
	v_pk_fma_f32 v[98:99], v[98:99], v[144:145], v[176:177]
	global_store_dwordx4 v[212:213], v[98:101], off
	s_waitcnt vmcnt(7)
	v_pk_fma_f32 v[92:93], v[92:93], v[156:157], v[182:183]
	v_pk_fma_f32 v[90:91], v[90:91], v[154:155], v[180:181]
	global_store_dwordx4 v[212:213], v[90:93], off offset:64
	s_waitcnt vmcnt(7)
	v_pk_fma_f32 v[88:89], v[88:89], v[162:163], v[186:187]
	v_pk_fma_f32 v[86:87], v[86:87], v[160:161], v[184:185]
	global_store_dwordx4 v[212:213], v[86:89], off offset:512
	s_waitcnt vmcnt(7)
	v_pk_fma_f32 v[80:81], v[80:81], v[174:175], v[194:195]
	v_pk_fma_f32 v[78:79], v[78:79], v[172:173], v[192:193]
	global_store_dwordx4 v[212:213], v[78:81], off offset:576
	s_waitcnt vmcnt(7)
	v_pk_fma_f32 v[84:85], v[84:85], v[146:147], v[198:199]
	v_pk_fma_f32 v[82:83], v[82:83], v[144:145], v[196:197]
	global_store_dwordx4 v[214:215], v[82:85], off
	s_waitcnt vmcnt(7)
	v_pk_fma_f32 v[76:77], v[76:77], v[156:157], v[202:203]
	v_pk_fma_f32 v[74:75], v[74:75], v[154:155], v[200:201]
	global_store_dwordx4 v[214:215], v[74:77], off offset:64
	s_waitcnt vmcnt(7)
	v_pk_fma_f32 v[72:73], v[72:73], v[162:163], v[206:207]
	v_pk_fma_f32 v[70:71], v[70:71], v[160:161], v[204:205]
	global_store_dwordx4 v[214:215], v[70:73], off offset:512
	s_waitcnt vmcnt(7)
	v_pk_fma_f32 v[68:69], v[68:69], v[174:175], v[210:211]
	v_pk_fma_f32 v[66:67], v[66:67], v[172:173], v[208:209]
	global_store_dwordx4 v[214:215], v[66:69], off offset:576
	v_add_co_u32_e32 v164, vcc, 0x100000, v166
	s_nop 1
	v_addc_co_u32_e32 v165, vcc, 0, v167, vcc
	global_load_dwordx4 v[176:179], v[164:165], off
	global_load_dwordx4 v[180:183], v[164:165], off offset:64
	global_load_dwordx4 v[184:187], v[164:165], off offset:512
	global_load_dwordx4 v[192:195], v[164:165], off offset:576
	v_add_co_u32_e32 v188, vcc, 0x120000, v166
	s_nop 1
	v_addc_co_u32_e32 v189, vcc, 0, v167, vcc
	global_load_dwordx4 v[196:199], v[188:189], off
	global_load_dwordx4 v[200:203], v[188:189], off offset:64
	global_load_dwordx4 v[204:207], v[188:189], off offset:512
	global_load_dwordx4 v[208:211], v[188:189], off offset:576
	v_add_co_u32_e32 v212, vcc, 0x100000, v170
	s_nop 1
	v_addc_co_u32_e32 v213, vcc, 0, v171, vcc
	v_add_co_u32_e32 v214, vcc, 0x120000, v170
	s_nop 1
	v_addc_co_u32_e32 v215, vcc, 0, v171, vcc
	s_waitcnt vmcnt(7)
	v_pk_fma_f32 v[64:65], v[64:65], v[146:147], v[178:179]
	v_pk_fma_f32 v[62:63], v[62:63], v[144:145], v[176:177]
	global_store_dwordx4 v[212:213], v[62:65], off
	s_waitcnt vmcnt(7)
	v_pk_fma_f32 v[60:61], v[60:61], v[156:157], v[182:183]
	v_pk_fma_f32 v[58:59], v[58:59], v[154:155], v[180:181]
	global_store_dwordx4 v[212:213], v[58:61], off offset:64
	s_waitcnt vmcnt(7)
	v_pk_fma_f32 v[56:57], v[56:57], v[162:163], v[186:187]
	v_pk_fma_f32 v[54:55], v[54:55], v[160:161], v[184:185]
	global_store_dwordx4 v[212:213], v[54:57], off offset:512
	s_waitcnt vmcnt(7)
	v_pk_fma_f32 v[48:49], v[48:49], v[174:175], v[194:195]
	v_pk_fma_f32 v[46:47], v[46:47], v[172:173], v[192:193]
	global_store_dwordx4 v[212:213], v[46:49], off offset:576
	s_waitcnt vmcnt(7)
	v_pk_fma_f32 v[52:53], v[52:53], v[146:147], v[198:199]
	v_pk_fma_f32 v[50:51], v[50:51], v[144:145], v[196:197]
	global_store_dwordx4 v[214:215], v[50:53], off
	s_waitcnt vmcnt(7)
	v_pk_fma_f32 v[44:45], v[44:45], v[156:157], v[202:203]
	v_pk_fma_f32 v[42:43], v[42:43], v[154:155], v[200:201]
	global_store_dwordx4 v[214:215], v[42:45], off offset:64
	s_waitcnt vmcnt(7)
	v_pk_fma_f32 v[40:41], v[40:41], v[162:163], v[206:207]
	v_pk_fma_f32 v[38:39], v[38:39], v[160:161], v[204:205]
	global_store_dwordx4 v[214:215], v[38:41], off offset:512
	s_waitcnt vmcnt(7)
	v_pk_fma_f32 v[32:33], v[32:33], v[174:175], v[210:211]
	v_pk_fma_f32 v[30:31], v[30:31], v[172:173], v[208:209]
	global_store_dwordx4 v[214:215], v[30:33], off offset:576
	v_add_co_u32_e32 v164, vcc, 0x140000, v166
	s_nop 1
	v_addc_co_u32_e32 v165, vcc, 0, v167, vcc
	global_load_dwordx4 v[176:179], v[164:165], off
	global_load_dwordx4 v[180:183], v[164:165], off offset:64
	global_load_dwordx4 v[184:187], v[164:165], off offset:512
	global_load_dwordx4 v[192:195], v[164:165], off offset:576
	v_add_co_u32_e32 v188, vcc, 0x160000, v166
	s_nop 1
	v_addc_co_u32_e32 v189, vcc, 0, v167, vcc
	global_load_dwordx4 v[196:199], v[188:189], off
	global_load_dwordx4 v[200:203], v[188:189], off offset:64
	global_load_dwordx4 v[204:207], v[188:189], off offset:512
	global_load_dwordx4 v[208:211], v[188:189], off offset:576
	v_add_co_u32_e32 v212, vcc, 0x140000, v170
	s_nop 1
	v_addc_co_u32_e32 v213, vcc, 0, v171, vcc
	v_add_co_u32_e32 v214, vcc, 0x160000, v170
	s_nop 1
	v_addc_co_u32_e32 v215, vcc, 0, v171, vcc
	s_waitcnt vmcnt(7)
	v_pk_fma_f32 v[36:37], v[36:37], v[146:147], v[178:179]
	v_pk_fma_f32 v[34:35], v[34:35], v[144:145], v[176:177]
	global_store_dwordx4 v[212:213], v[34:37], off
	s_waitcnt vmcnt(7)
	v_pk_fma_f32 v[28:29], v[28:29], v[156:157], v[182:183]
	v_pk_fma_f32 v[26:27], v[26:27], v[154:155], v[180:181]
	global_store_dwordx4 v[212:213], v[26:29], off offset:64
	s_waitcnt vmcnt(7)
	v_pk_fma_f32 v[24:25], v[24:25], v[162:163], v[186:187]
	v_pk_fma_f32 v[22:23], v[22:23], v[160:161], v[184:185]
	global_store_dwordx4 v[212:213], v[22:25], off offset:512
	s_waitcnt vmcnt(7)
	v_pk_fma_f32 v[16:17], v[16:17], v[174:175], v[194:195]
	v_pk_fma_f32 v[14:15], v[14:15], v[172:173], v[192:193]
	global_store_dwordx4 v[212:213], v[14:17], off offset:576
	s_waitcnt vmcnt(7)
	v_pk_fma_f32 v[20:21], v[20:21], v[146:147], v[198:199]
	v_pk_fma_f32 v[18:19], v[18:19], v[144:145], v[196:197]
	global_store_dwordx4 v[214:215], v[18:21], off
	s_waitcnt vmcnt(7)
	v_pk_fma_f32 v[12:13], v[12:13], v[156:157], v[202:203]
	v_pk_fma_f32 v[10:11], v[10:11], v[154:155], v[200:201]
	global_store_dwordx4 v[214:215], v[10:13], off offset:64
	s_waitcnt vmcnt(7)
	v_pk_fma_f32 v[8:9], v[8:9], v[162:163], v[206:207]
	v_pk_fma_f32 v[6:7], v[6:7], v[160:161], v[204:205]
	global_store_dwordx4 v[214:215], v[6:9], off offset:512
	s_waitcnt vmcnt(7)
	v_pk_fma_f32 v[4:5], v[4:5], v[174:175], v[210:211]
	v_pk_fma_f32 v[2:3], v[2:3], v[172:173], v[208:209]
	global_store_dwordx4 v[214:215], v[2:5], off offset:576
	s_mov_b32 s48, s12
	s_mov_b32 s20, s14
	s_mov_b64 s[24:25], s[18:19]
	s_mov_b64 s[22:23], s[16:17]
	v_readlane_b32 s50, v250, 9
	v_readlane_b32 s51, v250, 10
	v_readlane_b32 s54, v250, 13
	v_readlane_b32 s55, v250, 14
	v_readlane_b32 s56, v250, 15
	v_readlane_b32 s57, v250, 16
	v_readlane_b32 s58, v250, 17
	v_readlane_b32 s59, v250, 18
	v_readlane_b32 s60, v250, 19
	v_readlane_b32 s61, v250, 20
	v_readlane_b32 s62, v250, 21
	v_readlane_b32 s63, v250, 22
	s_and_b64 vcc, exec, s[0:1]
	s_cbranch_vccz .LBB0_1284
	s_waitcnt vmcnt(0)
	s_cmpk_gt_u32 s30, 0xff
	s_cbranch_scc1 .LBB0_1291
	s_barrier

.LBB0_2065:
	s_cmp_lt_i32 s54, 11
	s_cselect_b64 s[6:7], -1, 0
	s_and_b64 s[0:1], s[6:7], s[0:1]
	s_andn2_b64 vcc, exec, s[0:1]
	s_cbranch_vccnz .LBB0_2083
	v_mov_b32_e32 v1, v248
	s_waitcnt vmcnt(11)
	v_mov_b32_e32 v2, v0
	v_readlane_b32 s26, v250, 1
	v_readlane_b32 s27, v250, 0
	v_readlane_b32 s0, v250, 39
	s_mov_b64 s[0:1], s[52:53]
	s_mov_b64 s[2:3], s[90:91]
	s_cmpk_gt_i32 s27, 0x47f
	v_readfirstlane_b32 s28, v0
	s_barrier
	s_cbranch_scc1 .LBB0_2082
	s_add_u32 s8, s0, 0x2ec40000
	s_addc_u32 s9, s1, 0
	s_add_u32 s29, s0, 0x16940000
	s_addc_u32 s30, s1, 0
	s_add_u32 s10, s0, 0x1674000
	s_addc_u32 s11, s1, 0
	s_ashr_i32 s33, s27, 31
	s_lshr_b32 s5, s33, 29
	s_add_i32 s5, s27, s5
	s_lshr_b32 s4, s28, 6
	s_ashr_i32 s12, s5, 3
	s_and_b32 s5, s5, -8
	s_lshr_b32 s3, s28, 8
	s_lshl_b32 s31, s4, 10
	s_sub_i32 s5, s27, s5
	s_cmp_lt_i32 s5, 0
	s_movk_i32 s34, 0x91
	s_cselect_b32 s13, s34, 0x90
	s_mul_i32 s5, s13, s5
	s_add_i32 s5, s5, s12
	s_ashr_i32 s12, s5, 31
	s_lshr_b32 s12, s12, 26
	s_add_i32 s12, s5, s12
	s_ashr_i32 s13, s12, 6
	s_lshl_b32 s14, s13, 3
	s_sub_i32 s13, 0x90, s14
	s_min_u32 s15, s13, 8
	s_andn2_b32 s12, s12, 63
	s_sub_i32 s5, s5, s12
	v_cvt_f32_ubyte0_e32 v5, s15
	v_cvt_f32_i32_e32 v4, s5
	s_waitcnt vmcnt(10)
	v_rcp_iflag_f32_e32 v6, v5
	v_bfe_u32 v2, v0, 2, 4
	v_lshrrev_b32_e32 v3, 3, v0
	v_and_or_b32 v1, v3, 48, v2
	v_or_b32_e32 v3, 64, v3
	s_movk_i32 s2, 0x70
	v_and_or_b32 v150, v3, s2, v2
	v_mul_f32_e32 v2, v4, v6
	v_trunc_f32_e32 v2, v2
	v_fma_f32 v3, -v2, v5, v4
	v_cvt_i32_f32_e32 v2, v2
	s_ashr_i32 s2, s5, 30
	s_or_b32 s2, s2, 1
	v_cmp_ge_f32_e64 s[12:13], |v3|, v5
	s_and_b64 s[12:13], s[12:13], exec
	s_cselect_b32 s2, s2, 0
	v_readfirstlane_b32 s12, v2
	s_add_i32 s2, s12, s2
	s_mul_i32 s12, s2, s15
	s_sub_i32 s5, s5, s12
	s_sext_i32_i8 s5, s5
	s_add_i32 s46, s14, s5
	s_mul_hi_i32 s5, s46, 0x38e38e39
	s_lshr_b32 s12, s5, 31
	s_ashr_i32 s5, s5, 1
	s_add_i32 s12, s5, s12
	s_mul_i32 s5, s12, -9
	s_add_i32 s5, s5, s46
	s_mul_i32 s13, s12, 0x900
	s_lshl_b32 s5, s5, 8
	s_add_i32 s5, s5, s13
	v_or_b32_e32 v2, s5, v1
	v_or_b32_e32 v4, s5, v150
	s_bitset1_b32 s5, 7
	v_ashrrev_i32_e32 v3, 31, v2
	v_ashrrev_i32_e32 v5, 31, v4
	v_or_b32_e32 v6, s5, v1
	v_or_b32_e32 v8, s5, v150
	v_lshl_add_u64 v[2:3], v[2:3], 2, s[10:11]
	v_lshl_add_u64 v[4:5], v[4:5], 2, s[10:11]
	v_ashrrev_i32_e32 v7, 31, v6
	v_ashrrev_i32_e32 v9, 31, v8
	v_lshl_add_u64 v[6:7], v[6:7], 2, s[10:11]
	v_lshl_add_u64 v[8:9], v[8:9], 2, s[10:11]
	global_load_dword v2, v[2:3], off
	s_nop 0
	global_load_dword v3, v[4:5], off
	s_nop 0
	global_load_dword v4, v[6:7], off
	global_load_dword v5, v[8:9], off
	s_bfe_i64 s[14:15], s[2:3], 0x80000
	s_ashr_i32 s13, s12, 31
	s_lshl_b64 s[14:15], s[14:15], 20
	s_lshl_b64 s[12:13], s[12:13], 23
	s_add_u32 s5, s29, s12
	v_lshlrev_b32_e32 v6, 4, v0
	v_and_b32_e32 v7, 32, v0
	s_addc_u32 s12, s30, s13
	v_bitop3_b32 v6, v6, v7, 48 bitop3:0x6c
	s_add_u32 s20, s5, s14
	v_and_or_b32 v151, v0, 64, v6
	s_addc_u32 s21, s12, s15
	s_add_i32 s35, s31, 0
	v_lshl_or_b32 v132, v1, 12, v151
	s_add_i32 m0, s35, 0x10000
	v_lshl_or_b32 v130, v150, 12, v151
	global_load_lds_dwordx4 v132, s[20:21]
	s_add_i32 m0, s35, 0x12000
	s_add_i32 s36, s35, 0x2000
	global_load_lds_dwordx4 v130, s[20:21]
	s_mov_b32 m0, s35
	s_add_u32 s12, s20, 0x80000
	s_addc_u32 s13, s21, 0
	s_add_i32 s37, s35, 0x4000
	s_add_i32 s38, s35, 0x6000
	v_mov_b32_e32 v135, 0
	v_mov_b32_e32 v133, v135
	v_mov_b32_e32 v131, v135
	s_mov_b32 s39, 0
	v_mov_b32_e32 v141, v135
	s_waitcnt vmcnt(0)
	v_lshl_or_b32 v134, v2, 12, v151
	v_lshl_or_b32 v140, v3, 12, v151
	global_load_lds_dwordx4 v134, s[8:9]
	s_mov_b32 m0, s36
	v_lshl_or_b32 v142, v4, 12, v151
	global_load_lds_dwordx4 v140, s[8:9]
	s_add_i32 m0, s35, 0x14000
	v_lshl_or_b32 v144, v5, 12, v151
	global_load_lds_dwordx4 v132, s[12:13]
	s_add_i32 m0, s35, 0x16000
	v_lshl_add_u64 v[4:5], s[20:21], 0, v[132:133]
	global_load_lds_dwordx4 v130, s[12:13]
	s_mov_b32 m0, s37
	v_lshl_add_u64 v[2:3], s[20:21], 0, v[130:131]
	global_load_lds_dwordx4 v142, s[8:9]
	s_mov_b32 m0, s38
	s_cmp_lg_u32 s3, 1
	global_load_lds_dwordx4 v144, s[8:9]
	s_cbranch_scc1 .LBB0_2069
	s_barrier
	s_setprio 1

.LBB0_2133:
	s_cmp_lt_i32 s54, 12
	s_cselect_b64 s[6:7], -1, 0
	s_and_b64 s[0:1], s[6:7], s[0:1]
	s_andn2_b64 vcc, exec, s[0:1]
	s_cbranch_vccnz .LBB0_2151
	v_mov_b32_e32 v1, v248
	s_waitcnt vmcnt(11)
	v_mov_b32_e32 v2, v0
	v_readlane_b32 s20, v250, 1
	v_readlane_b32 s21, v250, 0
	v_readlane_b32 s0, v250, 39
	s_mov_b64 s[0:1], s[52:53]
	s_mov_b64 s[2:3], s[90:91]
	s_cmpk_gt_i32 s21, 0x47f
	v_readfirstlane_b32 s22, v0
	s_barrier
	s_cbranch_scc1 .LBB0_2150
	v_lshlrev_b32_e32 v1, 4, v0
	s_waitcnt vmcnt(9)
	v_or_b32_e32 v10, 0x2000, v1
	v_and_b32_e32 v4, 32, v0
	v_lshrrev_b32_e32 v2, 7, v10
	v_bfe_u32 v13, v0, 2, 4
	s_movk_i32 s2, 0x70
	v_bitop3_b32 v11, v1, v4, 48 bitop3:0x6c
	v_and_b32_e32 v12, 64, v0
	s_add_u32 s23, s0, 0x32d40000
	v_and_or_b32 v3, v2, s2, v13
	v_or_b32_e32 v1, v11, v12
	s_addc_u32 s24, s1, 0
	v_lshl_or_b32 v130, v3, 11, v1
	v_lshrrev_b32_e32 v3, 5, v0
	v_lshrrev_b32_e32 v5, 1, v0
	s_add_u32 s25, s0, 0x1e940000
	v_and_b32_e32 v3, 4, v3
	v_bfe_u32 v4, v0, 2, 2
	s_waitcnt vmcnt(8)
	v_and_b32_e32 v14, 24, v5
	s_addc_u32 s26, s1, 0
	v_or3_b32 v3, v3, v4, v14
	s_movk_i32 s2, 0x60
	s_ashr_i32 s28, s21, 31
	v_and_or_b32 v2, v2, s2, v3
	s_lshr_b32 s2, s28, 29
	s_add_i32 s2, s21, s2
	s_lshr_b32 s4, s22, 6
	s_ashr_i32 s5, s2, 3
	s_and_b32 s2, s2, -8
	s_lshr_b32 s3, s22, 8
	s_lshl_b32 s27, s4, 10
	s_sub_i32 s2, s21, s2
	s_cmp_lt_i32 s2, 0
	s_movk_i32 s29, 0x91
	s_cselect_b32 s8, s29, 0x90
	s_mul_i32 s2, s8, s2
	s_add_i32 s2, s2, s5
	s_ashr_i32 s5, s2, 31
	s_lshr_b32 s5, s5, 26
	s_add_i32 s5, s2, s5
	s_ashr_i32 s8, s5, 6
	s_lshl_b32 s10, s8, 3
	v_lshl_or_b32 v132, v2, 11, v1
	v_lshrrev_b32_e32 v2, 3, v0
	s_sub_i32 s8, 0x90, s10
	v_and_or_b32 v4, v2, 48, v13
	s_min_u32 s11, s8, 8
	s_andn2_b32 s5, s5, 63
	v_lshl_or_b32 v134, v4, 11, v1
	s_sub_i32 s5, s2, s5
	v_cvt_f32_ubyte0_e32 v4, s11
	v_and_or_b32 v2, v2, 32, v3
	v_cvt_f32_i32_e32 v3, s5
	v_rcp_iflag_f32_e32 v5, v4
	v_lshl_or_b32 v136, v2, 11, v1
	s_ashr_i32 s2, s5, 30
	s_or_b32 s2, s2, 1
	v_mul_f32_e32 v1, v3, v5
	v_trunc_f32_e32 v1, v1
	v_fma_f32 v2, -v1, v4, v3
	v_cvt_i32_f32_e32 v1, v1
	v_cmp_ge_f32_e64 s[8:9], |v2|, v4
	s_and_b64 s[8:9], s[8:9], exec
	s_cselect_b32 s2, s2, 0
	v_readfirstlane_b32 s8, v1
	s_add_i32 s2, s8, s2
	s_mul_i32 s8, s2, s11
	s_sub_i32 s5, s5, s8
	s_sext_i32_i8 s5, s5
	s_add_i32 s43, s10, s5
	s_mul_hi_i32 s5, s43, 0x38e38e39
	s_lshr_b32 s8, s5, 31
	s_ashr_i32 s5, s5, 1
	s_add_i32 s8, s5, s8
	s_mul_i32 s5, s8, -9
	s_add_i32 s5, s5, s43
	s_mul_i32 s9, s8, 0x900
	s_lshl_b32 s5, s5, 8
	s_add_i32 s10, s5, s9
	s_ashr_i32 s11, s10, 31
	s_lshl_b64 s[10:11], s[10:11], 11
	s_add_u32 s14, s23, s10
	s_addc_u32 s15, s24, s11
	s_ashr_i32 s9, s8, 31
	s_bfe_i64 s[10:11], s[2:3], 0x80000
	s_lshl_b64 s[10:11], s[10:11], 19
	s_lshl_b64 s[8:9], s[8:9], 22
	s_add_u32 s5, s25, s8
	s_addc_u32 s8, s26, s9
	s_add_u32 s16, s5, s10
	s_addc_u32 s17, s8, s11
	s_add_i32 s30, s27, 0
	s_add_i32 m0, s30, 0x10000
	s_add_i32 s31, s30, 0x2000
	global_load_lds_dwordx4 v136, s[16:17]
	s_add_i32 m0, s30, 0x12000
	s_add_u32 s8, s16, 0x40000
	global_load_lds_dwordx4 v132, s[16:17]
	s_mov_b32 m0, s30
	s_addc_u32 s9, s17, 0
	global_load_lds_dwordx4 v134, s[14:15]
	s_mov_b32 m0, s31
	v_mov_b32_e32 v137, 0
	global_load_lds_dwordx4 v130, s[14:15]
	s_add_i32 m0, s30, 0x14000
	v_mov_b32_e32 v133, v137
	global_load_lds_dwordx4 v136, s[8:9]
	s_add_i32 m0, s30, 0x16000
	v_mov_b32_e32 v135, v137
	global_load_lds_dwordx4 v132, s[8:9]
	s_add_u32 s8, s14, 0x40000
	s_addc_u32 s9, s15, 0
	s_add_i32 s33, s30, 0x4000
	s_mov_b32 m0, s33
	s_add_i32 s34, s30, 0x6000
	global_load_lds_dwordx4 v134, s[8:9]
	s_mov_b32 m0, s34
	v_mov_b32_e32 v131, v137
	global_load_lds_dwordx4 v130, s[8:9]
	s_mov_b32 s35, 0
	v_lshl_add_u64 v[8:9], s[16:17], 0, v[136:137]
	v_lshl_add_u64 v[6:7], s[16:17], 0, v[132:133]
	v_lshl_add_u64 v[4:5], s[14:15], 0, v[134:135]
	s_cmp_lg_u32 s3, 1
	v_lshl_add_u64 v[2:3], s[14:15], 0, v[130:131]
	s_cbranch_scc1 .LBB0_2137
	s_barrier
	s_setprio 1

.LBB0_2276:
	s_or_b64 exec, exec, s[8:9]
	s_cmpk_gt_i32 s33, 0x40f
	v_readfirstlane_b32 s41, v0
	s_waitcnt lgkmcnt(0)
	s_barrier
	s_barrier
	s_cbranch_scc1 .LBB0_2288
	v_lshlrev_b32_e32 v1, 4, v0
	s_waitcnt vmcnt(11)
	v_bfe_u32 v2, v0, 3, 25
	v_and_b32_e32 v5, 32, v0
	v_or_b32_e32 v2, 64, v2
	v_bfe_u32 v3, v0, 2, 4
	s_movk_i32 s0, 0x70
	v_bitop3_b32 v1, v1, v5, 48 bitop3:0x6c
	s_add_u32 s42, s6, 0x1370000
	v_and_or_b32 v4, v2, s0, v3
	v_and_or_b32 v1, v0, 64, v1
	s_addc_u32 s43, s7, 0
	v_lshl_or_b32 v132, v4, 9, v1
	v_lshrrev_b32_e32 v4, 5, v0
	s_waitcnt vmcnt(10)
	v_lshrrev_b32_e32 v6, 1, v0
	s_add_u32 s44, s6, 0x950000
	v_and_b32_e32 v4, 4, v4
	v_bfe_u32 v5, v0, 2, 2
	s_waitcnt vmcnt(9)
	v_and_b32_e32 v10, 24, v6
	s_addc_u32 s45, s7, 0
	v_or3_b32 v4, v4, v5, v10
	s_movk_i32 s0, 0x60
	s_ashr_i32 s47, s33, 31
	v_and_or_b32 v2, v2, s0, v4
	s_lshr_b32 s0, s47, 29
	s_add_i32 s0, s33, s0
	s_lshr_b32 s8, s41, 6
	s_ashr_i32 s2, s0, 3
	s_and_b32 s0, s0, -8
	s_lshr_b32 s1, s41, 8
	s_lshl_b32 s46, s8, 10
	s_sub_i32 s0, s33, s0
	s_cmp_lt_i32 s0, 0
	s_movk_i32 s48, 0x83
	s_cselect_b32 s3, s48, 0x82
	s_mul_i32 s0, s3, s0
	s_add_i32 s0, s0, s2
	s_mul_hi_i32 s2, s0, 0x7e07e07f
	s_lshr_b32 s3, s2, 31
	s_ashr_i32 s2, s2, 8
	s_add_i32 s2, s2, s3
	s_lshl_b32 s3, s2, 3
	s_mulk_i32 s2, 0x208
	s_sub_i32 s2, s0, s2
	s_bfe_u32 s0, s2, 0x3001c
	s_add_i32 s9, s2, s0
	s_sext_i32_i16 s0, s9
	s_and_b32 s9, s9, 0xfff8
	s_sub_i32 s2, s2, s9
	s_sext_i32_i16 s2, s2
	s_add_i32 s18, s3, s2
	s_ashr_i32 s19, s18, 31
	s_lshr_b32 s0, s0, 3
	s_lshl_b64 s[2:3], s[18:19], 17
	s_add_u32 s20, s42, s2
	s_addc_u32 s21, s43, s3
	s_bfe_i64 s[2:3], s[0:1], 0x100000
	s_lshl_b64 s[2:3], s[2:3], 17
	v_lshl_or_b32 v134, v2, 9, v1
	v_lshrrev_b32_e32 v2, 3, v0
	s_add_u32 s22, s44, s2
	v_and_or_b32 v3, v2, 48, v3
	v_and_or_b32 v2, v2, 32, v4
	s_addc_u32 s23, s45, s3
	s_add_i32 s19, s46, 0
	v_lshl_or_b32 v138, v2, 9, v1
	s_add_i32 m0, s19, 0x10000
	v_lshl_or_b32 v136, v3, 9, v1
	global_load_lds_dwordx4 v138, s[22:23]
	s_add_i32 m0, s19, 0x12000
	s_add_i32 s49, s19, 0x2000
	global_load_lds_dwordx4 v134, s[22:23]
	s_mov_b32 m0, s19
	s_add_u32 s2, s22, 0x10000
	global_load_lds_dwordx4 v136, s[20:21]
	s_mov_b32 m0, s49
	s_addc_u32 s3, s23, 0
	global_load_lds_dwordx4 v132, s[20:21]
	s_add_i32 m0, s19, 0x14000
	v_mov_b32_e32 v139, 0
	global_load_lds_dwordx4 v138, s[2:3]
	s_add_i32 m0, s19, 0x16000
	v_mov_b32_e32 v135, v139
	global_load_lds_dwordx4 v134, s[2:3]
	s_add_u32 s2, s20, 0x10000
	s_addc_u32 s3, s21, 0
	s_add_i32 s50, s19, 0x4000
	s_mov_b32 m0, s50
	s_add_i32 s51, s19, 0x6000
	global_load_lds_dwordx4 v136, s[2:3]
	s_mov_b32 m0, s51
	v_mov_b32_e32 v137, v139
	global_load_lds_dwordx4 v132, s[2:3]
	v_mov_b32_e32 v133, v139
	s_mov_b32 s52, 0
	v_lshl_add_u64 v[8:9], s[22:23], 0, v[138:139]
	v_lshl_add_u64 v[6:7], s[22:23], 0, v[134:135]
	v_lshl_add_u64 v[4:5], s[20:21], 0, v[136:137]
	s_cmp_lg_u32 s1, 1
	v_lshl_add_u64 v[2:3], s[20:21], 0, v[132:133]
	s_cbranch_scc1 .LBB0_2279
	s_barrier
	s_setprio 1

.LBB0_3223:
	s_cmp_lt_i32 s54, 19
	s_cselect_b64 s[4:5], -1, 0
	s_and_b64 s[0:1], s[4:5], s[0:1]
	s_andn2_b64 vcc, exec, s[0:1]
	s_cbranch_vccnz .LBB0_3261
	v_mov_b32_e32 v1, v0
	s_waitcnt vmcnt(11)
	v_mov_b32_e32 v2, v248
	v_readlane_b32 s30, v250, 0
	v_readlane_b32 s0, v250, 39
	v_readlane_b32 s31, v250, 1
	s_mov_b64 s[0:1], s[90:91]
	s_mov_b64 s[6:7], s[52:53]
	v_lshlrev_b32_e32 v2, 4, v0
	v_and_b32_e32 v1, 32, v0
	v_or_b32_e32 v150, 0x2000, v2
	v_bfe_u32 v149, v0, 2, 4
	v_bitop3_b32 v1, v2, v1, 48 bitop3:0x6c
	v_and_b32_e32 v148, 64, v0
	v_lshrrev_b32_e32 v4, 3, v0
	v_lshrrev_b32_e32 v2, 7, v150
	s_movk_i32 s0, 0x70
	v_or_b32_e32 v3, v1, v148
	v_and_or_b32 v4, v4, 48, v149
	v_and_or_b32 v2, v2, s0, v149
	v_lshl_or_b32 v130, v4, 11, v3
	v_lshl_or_b32 v132, v2, 11, v3
	v_bfe_u32 v151, v0, 4, 2
	v_lshlrev_b32_e32 v2, 6, v0
	v_lshlrev_b32_e32 v3, 2, v0
	v_lshlrev_b32_e32 v153, 4, v151
	v_and_b32_e32 v2, 0x3c0, v2
	v_and_b32_e32 v3, 32, v3
	s_cmpk_lt_i32 s30, 0x200
	v_readfirstlane_b32 s33, v0
	v_and_b32_e32 v152, 15, v0
	s_cselect_b64 s[2:3], -1, 0
	s_cmpk_gt_i32 s30, 0x1ff
	v_bitop3_b32 v154, v153, v3, v2 bitop3:0x36
	s_barrier
	s_cbranch_scc1 .LBB0_3236
	s_add_u32 s34, s6, 0x3cf40000
	s_addc_u32 s35, s7, 0
	s_add_u32 s36, s6, 0x15540000
	s_addc_u32 s37, s7, 0
	s_ashr_i32 s39, s30, 31
	s_lshr_b32 s0, s39, 29
	s_add_i32 s0, s30, s0
	s_lshr_b32 s8, s33, 6
	s_ashr_i32 s9, s0, 3
	s_and_b32 s0, s0, -8
	s_lshr_b32 s1, s33, 8
	s_lshl_b32 s38, s8, 10
	s_sub_i32 s0, s30, s0
	s_cmp_lt_i32 s0, 0
	s_cselect_b32 s10, 0x41, 64
	s_mul_i32 s0, s10, s0
	s_add_i32 s0, s0, s9
	s_ashr_i32 s9, s0, 31
	s_lshr_b32 s9, s9, 26
	s_add_i32 s9, s0, s9
	s_ashr_i32 s10, s9, 6
	s_lshl_b32 s12, s10, 3
	s_sub_i32 s10, 64, s12
	s_min_u32 s13, s10, 8
	s_andn2_b32 s9, s9, 63
	s_sub_i32 s9, s0, s9
	v_cvt_f32_ubyte0_e32 v3, s13
	v_cvt_f32_i32_e32 v2, s9
	v_rcp_iflag_f32_e32 v4, v3
	s_ashr_i32 s0, s9, 30
	s_or_b32 s0, s0, 1
	v_mov_b32_e32 v131, 0
	v_mul_f32_e32 v4, v2, v4
	v_trunc_f32_e32 v4, v4
	v_fma_f32 v2, -v4, v3, v2
	v_cvt_i32_f32_e32 v4, v4
	v_cmp_ge_f32_e64 s[10:11], |v2|, v3
	s_and_b64 s[10:11], s[10:11], exec
	s_cselect_b32 s0, s0, 0
	v_readfirstlane_b32 s10, v4
	s_add_i32 s0, s10, s0
	s_mul_i32 s10, s0, s13
	s_sub_i32 s9, s9, s10
	s_sext_i32_i8 s9, s9
	s_add_i32 s22, s12, s9
	s_ashr_i32 s23, s22, 31
	s_lshl_b64 s[10:11], s[22:23], 19
	s_add_u32 s24, s34, s10
	s_addc_u32 s25, s35, s11
	s_bfe_i64 s[10:11], s[0:1], 0x80000
	s_lshl_b64 s[10:11], s[10:11], 19
	s_add_u32 s26, s36, s10
	s_addc_u32 s27, s37, s11
	s_add_i32 s23, s38, 0
	s_add_i32 m0, s23, 0x10000
	s_add_i32 s40, s23, 0x2000
	global_load_lds_dwordx4 v130, s[26:27]
	s_add_i32 m0, s23, 0x12000
	s_add_u32 s10, s26, 0x40000
	global_load_lds_dwordx4 v132, s[26:27]
	s_mov_b32 m0, s23
	s_addc_u32 s11, s27, 0
	global_load_lds_dwordx4 v130, s[24:25]
	s_mov_b32 m0, s40
	v_mov_b32_e32 v133, v131
	global_load_lds_dwordx4 v132, s[24:25]
	s_add_i32 m0, s23, 0x14000
	s_mov_b32 s43, 0
	global_load_lds_dwordx4 v130, s[10:11]
	s_add_i32 m0, s23, 0x16000
	s_waitcnt vmcnt(0)
	v_lshl_add_u64 v[8:9], s[26:27], 0, v[130:131]
	global_load_lds_dwordx4 v132, s[10:11]
	s_add_u32 s10, s24, 0x40000
	s_addc_u32 s11, s25, 0
	s_add_i32 s41, s23, 0x4000
	s_mov_b32 m0, s41
	s_add_i32 s42, s23, 0x6000
	global_load_lds_dwordx4 v130, s[10:11]
	s_mov_b32 m0, s42
	v_lshl_add_u64 v[6:7], s[26:27], 0, v[132:133]
	global_load_lds_dwordx4 v132, s[10:11]
	v_lshl_add_u64 v[4:5], s[24:25], 0, v[130:131]
	s_cmp_lg_u32 s1, 1
	v_lshl_add_u64 v[2:3], s[24:25], 0, v[132:133]
	s_cbranch_scc1 .LBB0_3227
	s_barrier
	s_setprio 1

.LBB0_3236:
	v_cndmask_b32_e64 v2, 0, 1, s[2:3]
	v_cmp_ne_u32_e64 s[0:1], 1, v2
	s_andn2_b64 vcc, exec, s[2:3]
	v_readfirstlane_b32 s33, v0
	s_cbranch_vccnz .LBB0_3248
	s_add_u32 s34, s6, 0x4e400000
	s_addc_u32 s35, s7, 0
	s_add_u32 s36, s6, 0x15940000
	s_addc_u32 s37, s7, 0
	s_ashr_i32 s39, s30, 31
	s_lshr_b32 s2, s39, 29
	s_add_i32 s2, s30, s2
	s_lshr_b32 s8, s33, 6
	s_ashr_i32 s9, s2, 3
	s_and_b32 s2, s2, -8
	s_lshr_b32 s3, s33, 8
	s_lshl_b32 s38, s8, 10
	s_sub_i32 s2, s30, s2
	s_cmp_lt_i32 s2, 0
	s_cselect_b32 s10, 0x41, 64
	s_mul_i32 s2, s10, s2
	s_add_i32 s2, s2, s9
	s_ashr_i32 s9, s2, 31
	s_lshr_b32 s9, s9, 26
	s_add_i32 s9, s2, s9
	s_ashr_i32 s10, s9, 6
	s_lshl_b32 s12, s10, 3
	s_sub_i32 s10, 64, s12
	s_min_u32 s13, s10, 8
	s_andn2_b32 s9, s9, 63
	s_sub_i32 s9, s2, s9
	v_cvt_f32_ubyte0_e32 v3, s13
	v_cvt_f32_i32_e32 v2, s9
	v_rcp_iflag_f32_e32 v4, v3
	s_ashr_i32 s2, s9, 30
	s_or_b32 s2, s2, 1
	v_mov_b32_e32 v131, 0
	v_mul_f32_e32 v4, v2, v4
	v_trunc_f32_e32 v4, v4
	v_fma_f32 v2, -v4, v3, v2
	v_cvt_i32_f32_e32 v4, v4
	v_cmp_ge_f32_e64 s[10:11], |v2|, v3
	s_and_b64 s[10:11], s[10:11], exec
	s_cselect_b32 s2, s2, 0
	v_readfirstlane_b32 s10, v4
	s_add_i32 s2, s10, s2
	s_mul_i32 s10, s2, s13
	s_sub_i32 s9, s9, s10
	s_sext_i32_i8 s9, s9
	s_add_i32 s22, s12, s9
	s_ashr_i32 s23, s22, 31
	s_lshl_b64 s[10:11], s[22:23], 19
	s_add_u32 s24, s34, s10
	s_addc_u32 s25, s35, s11
	s_bfe_i64 s[10:11], s[2:3], 0x80000
	s_lshl_b64 s[10:11], s[10:11], 19
	s_add_u32 s26, s36, s10
	s_addc_u32 s27, s37, s11
	s_add_i32 s23, s38, 0
	s_add_i32 m0, s23, 0x10000
	s_add_i32 s40, s23, 0x2000
	global_load_lds_dwordx4 v130, s[26:27]
	s_add_i32 m0, s23, 0x12000
	s_add_u32 s10, s26, 0x40000
	global_load_lds_dwordx4 v132, s[26:27]
	s_mov_b32 m0, s23
	s_addc_u32 s11, s27, 0
	global_load_lds_dwordx4 v130, s[24:25]
	s_mov_b32 m0, s40
	v_mov_b32_e32 v133, v131
	global_load_lds_dwordx4 v132, s[24:25]
	s_add_i32 m0, s23, 0x14000
	s_mov_b32 s43, 0
	global_load_lds_dwordx4 v130, s[10:11]
	s_add_i32 m0, s23, 0x16000
	s_waitcnt vmcnt(0)
	v_lshl_add_u64 v[8:9], s[26:27], 0, v[130:131]
	global_load_lds_dwordx4 v132, s[10:11]
	s_add_u32 s10, s24, 0x40000
	s_addc_u32 s11, s25, 0
	s_add_i32 s41, s23, 0x4000
	s_mov_b32 m0, s41
	s_add_i32 s42, s23, 0x6000
	global_load_lds_dwordx4 v130, s[10:11]
	s_mov_b32 m0, s42
	v_lshl_add_u64 v[6:7], s[26:27], 0, v[132:133]
	global_load_lds_dwordx4 v132, s[10:11]
	v_lshl_add_u64 v[4:5], s[24:25], 0, v[130:131]
	s_cmp_lg_u32 s3, 1
	v_lshl_add_u64 v[2:3], s[24:25], 0, v[132:133]
	s_cbranch_scc1 .LBB0_3239
	s_barrier
	s_setprio 1

.LBB0_3248:
	s_and_b64 vcc, exec, s[0:1]
	v_readfirstlane_b32 s28, v0
	s_cbranch_vccnz .LBB0_3260
	s_add_u32 s29, s6, 0x50480000
	s_addc_u32 s33, s7, 0
	s_add_u32 s34, s6, 0x15d40000
	s_addc_u32 s35, s7, 0
	s_ashr_i32 s37, s30, 31
	s_lshr_b32 s0, s37, 29
	s_add_i32 s0, s30, s0
	s_lshr_b32 s2, s28, 6
	s_ashr_i32 s3, s0, 3
	s_and_b32 s0, s0, -8
	s_lshr_b32 s1, s28, 8
	s_lshl_b32 s36, s2, 10
	s_sub_i32 s0, s30, s0
	s_cmp_lt_i32 s0, 0
	s_cselect_b32 s8, 0x41, 64
	s_mul_i32 s0, s8, s0
	s_add_i32 s0, s0, s3
	s_ashr_i32 s3, s0, 31
	s_lshr_b32 s3, s3, 26
	s_add_i32 s3, s0, s3
	s_ashr_i32 s8, s3, 6
	s_lshl_b32 s10, s8, 3
	s_sub_i32 s8, 64, s10
	s_min_u32 s11, s8, 8
	s_andn2_b32 s3, s3, 63
	s_sub_i32 s3, s0, s3
	v_cvt_f32_ubyte0_e32 v3, s11
	v_cvt_f32_i32_e32 v2, s3
	v_rcp_iflag_f32_e32 v4, v3
	s_ashr_i32 s0, s3, 30
	s_or_b32 s0, s0, 1
	v_mov_b32_e32 v131, 0
	v_mul_f32_e32 v4, v2, v4
	v_trunc_f32_e32 v4, v4
	v_fma_f32 v2, -v4, v3, v2
	v_cvt_i32_f32_e32 v4, v4
	v_cmp_ge_f32_e64 s[8:9], |v2|, v3
	s_and_b64 s[8:9], s[8:9], exec
	s_cselect_b32 s0, s0, 0
	v_readfirstlane_b32 s8, v4
	s_add_i32 s0, s8, s0
	s_mul_i32 s8, s0, s11
	s_sub_i32 s3, s3, s8
	s_sext_i32_i8 s3, s3
	s_add_i32 s20, s10, s3
	s_ashr_i32 s21, s20, 31
	s_lshl_b64 s[8:9], s[20:21], 19
	s_add_u32 s22, s29, s8
	s_addc_u32 s23, s33, s9
	s_bfe_i64 s[8:9], s[0:1], 0x80000
	s_lshl_b64 s[8:9], s[8:9], 19
	s_add_u32 s24, s34, s8
	s_addc_u32 s25, s35, s9
	s_add_i32 s21, s36, 0
	s_add_i32 m0, s21, 0x10000
	s_add_i32 s38, s21, 0x2000
	global_load_lds_dwordx4 v130, s[24:25]
	s_add_i32 m0, s21, 0x12000
	s_add_u32 s8, s24, 0x40000
	global_load_lds_dwordx4 v132, s[24:25]
	s_mov_b32 m0, s21
	s_addc_u32 s9, s25, 0
	global_load_lds_dwordx4 v130, s[22:23]
	s_mov_b32 m0, s38
	v_mov_b32_e32 v133, v131
	global_load_lds_dwordx4 v132, s[22:23]
	s_add_i32 m0, s21, 0x14000
	s_mov_b32 s41, 0
	global_load_lds_dwordx4 v130, s[8:9]
	s_add_i32 m0, s21, 0x16000
	s_waitcnt vmcnt(0)
	v_lshl_add_u64 v[8:9], s[24:25], 0, v[130:131]
	global_load_lds_dwordx4 v132, s[8:9]
	s_add_u32 s8, s22, 0x40000
	s_addc_u32 s9, s23, 0
	s_add_i32 s39, s21, 0x4000
	s_mov_b32 m0, s39
	s_add_i32 s40, s21, 0x6000
	global_load_lds_dwordx4 v130, s[8:9]
	s_mov_b32 m0, s40
	v_lshl_add_u64 v[6:7], s[24:25], 0, v[132:133]
	global_load_lds_dwordx4 v132, s[8:9]
	v_lshl_add_u64 v[4:5], s[22:23], 0, v[130:131]
	s_cmp_lg_u32 s1, 1
	v_lshl_add_u64 v[2:3], s[22:23], 0, v[132:133]
	s_cbranch_scc1 .LBB0_3251
	s_barrier
	s_setprio 1

.LBB0_3311:
	s_cmp_lt_i32 s54, 20
	s_cselect_b64 s[2:3], -1, 0
	s_and_b64 s[0:1], s[2:3], s[0:1]
	s_andn2_b64 vcc, exec, s[0:1]
	s_cbranch_vccnz .LBB0_3325
	v_mov_b32_e32 v1, v0
	s_waitcnt vmcnt(11)
	v_mov_b32_e32 v2, v248
	v_readlane_b32 s33, v250, 0
	v_readlane_b32 s0, v250, 39
	v_readlane_b32 s40, v250, 1
	s_mov_b64 s[4:5], s[52:53]
	s_mov_b64 s[0:1], s[90:91]
	s_cmpk_gt_i32 s33, 0x1ff
	v_readfirstlane_b32 s41, v0
	s_barrier
	s_cbranch_scc1 .LBB0_3324
	s_add_u32 s42, s4, 0x2ab40000
	s_addc_u32 s43, s5, 0
	v_lshlrev_b32_e32 v1, 4, v0
	s_add_u32 s44, s4, 0x16140000
	s_waitcnt vmcnt(9)
	v_or_b32_e32 v10, 0x2000, v1
	s_addc_u32 s45, s5, 0
	v_lshrrev_b32_e32 v2, 7, v10
	v_bfe_u32 v13, v0, 2, 4
	s_movk_i32 s0, 0x70
	s_ashr_i32 s47, s33, 31
	v_and_or_b32 v2, v2, s0, v13
	s_lshr_b32 s0, s47, 29
	s_add_i32 s0, s33, s0
	s_ashr_i32 s7, s0, 3
	s_and_b32 s0, s0, -8
	s_sub_i32 s0, s33, s0
	s_lshr_b32 s8, s0, 31
	s_or_b32 s8, s8, 64
	s_mul_i32 s0, s8, s0
	s_add_i32 s0, s0, s7
	s_ashr_i32 s7, s0, 31
	s_lshr_b32 s7, s7, 26
	s_add_i32 s7, s0, s7
	s_ashr_i32 s8, s7, 6
	s_lshl_b32 s10, s8, 3
	s_sub_i32 s8, 64, s10
	s_min_u32 s11, s8, 8
	s_andn2_b32 s7, s7, 63
	v_and_b32_e32 v3, 32, v0
	s_sub_i32 s7, s0, s7
	v_cvt_f32_ubyte0_e32 v4, s11
	v_bitop3_b32 v11, v1, v3, 48 bitop3:0x6c
	v_and_b32_e32 v12, 64, v0
	v_cvt_f32_i32_e32 v3, s7
	v_rcp_iflag_f32_e32 v5, v4
	v_or_b32_e32 v1, v11, v12
	v_lshl_or_b32 v130, v2, 12, v1
	v_lshrrev_b32_e32 v2, 3, v0
	v_and_or_b32 v2, v2, 48, v13
	v_lshl_or_b32 v132, v2, 12, v1
	v_mul_f32_e32 v1, v3, v5
	v_trunc_f32_e32 v1, v1
	v_fma_f32 v2, -v1, v4, v3
	v_cvt_i32_f32_e32 v1, v1
	s_lshr_b32 s6, s41, 6
	s_ashr_i32 s0, s7, 30
	s_lshr_b32 s1, s41, 8
	s_lshl_b32 s46, s6, 10
	s_or_b32 s0, s0, 1
	v_cmp_ge_f32_e64 s[8:9], |v2|, v4
	s_and_b64 s[8:9], s[8:9], exec
	s_cselect_b32 s0, s0, 0
	v_readfirstlane_b32 s8, v1
	s_add_i32 s0, s8, s0
	s_mul_i32 s8, s0, s11
	s_sub_i32 s7, s7, s8
	s_sext_i32_i8 s7, s7
	s_add_i32 s30, s10, s7
	s_ashr_i32 s31, s30, 31
	s_lshl_b64 s[8:9], s[30:31], 20
	s_add_u32 s34, s42, s8
	s_addc_u32 s35, s43, s9
	s_bfe_i64 s[8:9], s[0:1], 0x80000
	s_lshl_b64 s[8:9], s[8:9], 20
	s_add_u32 s36, s44, s8
	s_addc_u32 s37, s45, s9
	s_add_i32 s31, s46, 0
	s_add_i32 m0, s31, 0x10000
	s_add_i32 s48, s31, 0x2000
	global_load_lds_dwordx4 v132, s[36:37]
	s_add_i32 m0, s31, 0x12000
	s_add_u32 s8, s36, 0x80000
	global_load_lds_dwordx4 v130, s[36:37]
	s_mov_b32 m0, s31
	s_addc_u32 s9, s37, 0
	global_load_lds_dwordx4 v132, s[34:35]
	s_mov_b32 m0, s48
	v_mov_b32_e32 v135, 0
	global_load_lds_dwordx4 v130, s[34:35]
	s_add_i32 m0, s31, 0x14000
	v_mov_b32_e32 v133, v135
	global_load_lds_dwordx4 v132, s[8:9]
	s_add_i32 m0, s31, 0x16000
	v_mov_b32_e32 v131, v135
	global_load_lds_dwordx4 v130, s[8:9]
	s_add_u32 s8, s34, 0x80000
	s_addc_u32 s9, s35, 0
	s_add_i32 s49, s31, 0x4000
	s_mov_b32 m0, s49
	s_add_i32 s50, s31, 0x6000
	global_load_lds_dwordx4 v132, s[8:9]
	s_mov_b32 m0, s50
	s_mov_b32 s51, 0
	global_load_lds_dwordx4 v130, s[8:9]
	v_lshl_add_u64 v[8:9], s[36:37], 0, v[132:133]
	v_lshl_add_u64 v[6:7], s[36:37], 0, v[130:131]
	v_lshl_add_u64 v[4:5], s[34:35], 0, v[132:133]
	s_cmp_lg_u32 s1, 1
	v_lshl_add_u64 v[2:3], s[34:35], 0, v[130:131]
	s_cbranch_scc1 .LBB0_3315
	s_barrier
	s_setprio 1

.LBB0_3319:
	ds_read_b128 v[144:147], v152
	ds_read_b128 v[158:161], v152 offset:1024
	ds_read_b128 v[162:165], v152 offset:2048
	ds_read_b128 v[166:169], v152 offset:3072
	s_add_u32 s36, s34, 0xfff80080
	s_addc_u32 s37, s35, -1
	s_cmp_eq_u32 s69, 28
	s_cselect_b32 s39, s25, s37
	s_cselect_b32 s38, s65, s36
	s_cselect_b32 s37, s23, s68
	s_cselect_b32 s36, s66, s67
	v_lshl_add_u64 v[148:149], s[34:35], 0, v[136:137]
	s_add_i32 m0, s31, 0xc000
	ds_read_b128 v[170:173], v153
	ds_read_b128 v[174:177], v153 offset:1024
	ds_read_b128 v[178:181], v153 offset:2048
	ds_read_b128 v[182:185], v153 offset:3072
	ds_read_b128 v[186:189], v153 offset:4096
	ds_read_b128 v[190:193], v153 offset:5120
	ds_read_b128 v[194:197], v153 offset:6144
	ds_read_b128 v[198:201], v153 offset:7168
	global_load_lds_dwordx4 v[148:149], off
	v_lshl_add_u64 v[148:149], s[34:35], 0, v[138:139]
	s_add_i32 m0, s31, 0xe000
	s_nop 0
	global_load_lds_dwordx4 v[148:149], off
	s_waitcnt lgkmcnt(8)
	s_barrier
	s_waitcnt lgkmcnt(0)
	s_waitcnt lgkmcnt(0)
	v_mfma_f32_16x16x32_bf16 v[126:129], v[144:147], v[170:173], v[126:129]
	v_mfma_f32_16x16x32_bf16 v[122:125], v[162:165], v[170:173], v[122:125]
	v_mfma_f32_16x16x32_bf16 v[110:113], v[144:147], v[178:181], v[110:113]
	v_mfma_f32_16x16x32_bf16 v[106:109], v[162:165], v[178:181], v[106:109]
	v_mfma_f32_16x16x32_bf16 v[94:97], v[144:147], v[186:189], v[94:97]
	v_mfma_f32_16x16x32_bf16 v[90:93], v[162:165], v[186:189], v[90:93]
	v_mfma_f32_16x16x32_bf16 v[78:81], v[144:147], v[194:197], v[78:81]
	v_mfma_f32_16x16x32_bf16 v[74:77], v[162:165], v[194:197], v[74:77]
	v_mfma_f32_16x16x32_bf16 v[126:129], v[158:161], v[174:177], v[126:129]
	v_mfma_f32_16x16x32_bf16 v[122:125], v[166:169], v[174:177], v[122:125]
	v_mfma_f32_16x16x32_bf16 v[110:113], v[158:161], v[182:185], v[110:113]
	v_mfma_f32_16x16x32_bf16 v[106:109], v[166:169], v[182:185], v[106:109]
	v_mfma_f32_16x16x32_bf16 v[94:97], v[158:161], v[190:193], v[94:97]
	v_mfma_f32_16x16x32_bf16 v[90:93], v[166:169], v[190:193], v[90:93]
	v_mfma_f32_16x16x32_bf16 v[78:81], v[158:161], v[198:201], v[78:81]
	v_mfma_f32_16x16x32_bf16 v[74:77], v[166:169], v[198:201], v[74:77]
	s_barrier
	s_add_i32 s70, s55, s46
	v_lshl_add_u64 v[148:149], s[36:37], 0, v[132:133]
	s_mov_b32 m0, s70
	ds_read_b128 v[202:205], v154
	ds_read_b128 v[206:209], v154 offset:1024
	ds_read_b128 v[210:213], v154 offset:2048
	ds_read_b128 v[214:217], v154 offset:3072
	global_load_lds_dwordx4 v[148:149], off
	v_lshl_add_u64 v[218:219], s[36:37], 0, v[130:131]
	s_add_i32 m0, s70, 0x2000
	s_nop 0
	global_load_lds_dwordx4 v[218:219], off
	s_barrier
	s_waitcnt lgkmcnt(0)
	s_waitcnt lgkmcnt(0)
	v_mfma_f32_16x16x32_bf16 v[118:121], v[202:205], v[170:173], v[118:121]
	v_mfma_f32_16x16x32_bf16 v[114:117], v[210:213], v[170:173], v[114:117]
	v_mfma_f32_16x16x32_bf16 v[102:105], v[202:205], v[178:181], v[102:105]
	v_mfma_f32_16x16x32_bf16 v[98:101], v[210:213], v[178:181], v[98:101]
	v_mfma_f32_16x16x32_bf16 v[86:89], v[202:205], v[186:189], v[86:89]
	v_mfma_f32_16x16x32_bf16 v[82:85], v[210:213], v[186:189], v[82:85]
	v_mfma_f32_16x16x32_bf16 v[70:73], v[202:205], v[194:197], v[70:73]
	v_mfma_f32_16x16x32_bf16 v[66:69], v[210:213], v[194:197], v[66:69]
	v_mfma_f32_16x16x32_bf16 v[118:121], v[206:209], v[174:177], v[118:121]
	v_mfma_f32_16x16x32_bf16 v[114:117], v[214:217], v[174:177], v[114:117]
	v_mfma_f32_16x16x32_bf16 v[102:105], v[206:209], v[182:185], v[102:105]
	v_mfma_f32_16x16x32_bf16 v[98:101], v[214:217], v[182:185], v[98:101]
	v_mfma_f32_16x16x32_bf16 v[86:89], v[206:209], v[190:193], v[86:89]
	v_mfma_f32_16x16x32_bf16 v[82:85], v[214:217], v[190:193], v[82:85]
	v_mfma_f32_16x16x32_bf16 v[70:73], v[206:209], v[198:201], v[70:73]
	v_mfma_f32_16x16x32_bf16 v[66:69], v[214:217], v[198:201], v[66:69]
	s_mov_b32 m0, s31
	v_lshl_add_u64 v[220:221], s[38:39], 0, v[132:133]
	s_barrier
	ds_read_b128 v[170:173], v153 offset:16384
	ds_read_b128 v[174:177], v153 offset:17408
	ds_read_b128 v[178:181], v153 offset:18432
	ds_read_b128 v[182:185], v153 offset:19456
	ds_read_b128 v[186:189], v153 offset:20480
	ds_read_b128 v[190:193], v153 offset:21504
	ds_read_b128 v[194:197], v153 offset:22528
	ds_read_b128 v[198:201], v153 offset:23552
	global_load_lds_dwordx4 v[220:221], off
	v_lshl_add_u64 v[222:223], s[38:39], 0, v[130:131]
	s_mov_b32 m0, s48
	s_nop 0
	global_load_lds_dwordx4 v[222:223], off
	s_barrier
	s_waitcnt lgkmcnt(0)
	s_waitcnt lgkmcnt(0)
	v_mfma_f32_16x16x32_bf16 v[62:65], v[144:147], v[170:173], v[62:65]
	v_mfma_f32_16x16x32_bf16 v[58:61], v[162:165], v[170:173], v[58:61]
	v_mfma_f32_16x16x32_bf16 v[46:49], v[144:147], v[178:181], v[46:49]
	v_mfma_f32_16x16x32_bf16 v[42:45], v[162:165], v[178:181], v[42:45]
	v_mfma_f32_16x16x32_bf16 v[30:33], v[144:147], v[186:189], v[30:33]
	v_mfma_f32_16x16x32_bf16 v[26:29], v[162:165], v[186:189], v[26:29]
	v_mfma_f32_16x16x32_bf16 v[22:25], v[144:147], v[194:197], v[22:25]
	v_mfma_f32_16x16x32_bf16 v[14:17], v[162:165], v[194:197], v[14:17]
	v_mfma_f32_16x16x32_bf16 v[62:65], v[158:161], v[174:177], v[62:65]
	v_mfma_f32_16x16x32_bf16 v[58:61], v[166:169], v[174:177], v[58:61]
	v_mfma_f32_16x16x32_bf16 v[46:49], v[158:161], v[182:185], v[46:49]
	v_mfma_f32_16x16x32_bf16 v[42:45], v[166:169], v[182:185], v[42:45]
	v_mfma_f32_16x16x32_bf16 v[30:33], v[158:161], v[190:193], v[30:33]
	v_mfma_f32_16x16x32_bf16 v[26:29], v[166:169], v[190:193], v[26:29]
	v_mfma_f32_16x16x32_bf16 v[22:25], v[158:161], v[198:201], v[22:25]
	v_mfma_f32_16x16x32_bf16 v[14:17], v[166:169], v[198:201], v[14:17]
	s_barrier
	s_add_u32 s70, s36, 0x80000
	s_addc_u32 s71, s37, 0
	s_add_i32 s72, s56, s46
	v_lshl_add_u64 v[144:145], s[70:71], 0, v[132:133]
	s_mov_b32 m0, s72
	s_nop 0
	global_load_lds_dwordx4 v[144:145], off
	v_lshl_add_u64 v[144:145], s[70:71], 0, v[130:131]
	s_add_i32 m0, s72, 0x2000
	s_nop 0
	global_load_lds_dwordx4 v[144:145], off
	s_waitcnt vmcnt(6)
	s_barrier
	v_mfma_f32_16x16x32_bf16 v[54:57], v[202:205], v[170:173], v[54:57]
	v_mfma_f32_16x16x32_bf16 v[50:53], v[210:213], v[170:173], v[50:53]
	v_mfma_f32_16x16x32_bf16 v[38:41], v[202:205], v[178:181], v[38:41]
	v_mfma_f32_16x16x32_bf16 v[34:37], v[210:213], v[178:181], v[34:37]
	v_mfma_f32_16x16x32_bf16 v[18:21], v[202:205], v[186:189], v[18:21]
	v_mfma_f32_16x16x32_bf16 v[10:13], v[210:213], v[186:189], v[10:13]
	v_mfma_f32_16x16x32_bf16 v[6:9], v[202:205], v[194:197], v[6:9]
	v_mfma_f32_16x16x32_bf16 v[2:5], v[210:213], v[194:197], v[2:5]
	v_mfma_f32_16x16x32_bf16 v[54:57], v[206:209], v[174:177], v[54:57]
	v_mfma_f32_16x16x32_bf16 v[50:53], v[214:217], v[174:177], v[50:53]
	v_mfma_f32_16x16x32_bf16 v[38:41], v[206:209], v[182:185], v[38:41]
	v_mfma_f32_16x16x32_bf16 v[34:37], v[214:217], v[182:185], v[34:37]
	v_mfma_f32_16x16x32_bf16 v[18:21], v[206:209], v[190:193], v[18:21]
	v_mfma_f32_16x16x32_bf16 v[10:13], v[214:217], v[190:193], v[10:13]
	v_mfma_f32_16x16x32_bf16 v[6:9], v[206:209], v[198:201], v[6:9]
	v_mfma_f32_16x16x32_bf16 v[2:5], v[214:217], v[198:201], v[2:5]
	s_add_i32 s70, 0, 0x18000
	v_add_u32_e32 v134, s70, v150
	s_barrier
	ds_read_b128 v[144:147], v134
	ds_read_b128 v[158:161], v134 offset:1024
	ds_read_b128 v[162:165], v134 offset:2048
	ds_read_b128 v[166:169], v134 offset:3072
	s_add_u32 s38, s38, 0x80000
	s_addc_u32 s39, s39, 0
	s_mov_b32 m0, s49
	v_lshl_add_u64 v[202:203], s[38:39], 0, v[132:133]
	ds_read_b128 v[170:173], v153 offset:32768
	ds_read_b128 v[174:177], v153 offset:33792
	ds_read_b128 v[178:181], v153 offset:34816
	ds_read_b128 v[182:185], v153 offset:35840
	ds_read_b128 v[186:189], v153 offset:36864
	ds_read_b128 v[190:193], v153 offset:37888
	ds_read_b128 v[194:197], v153 offset:38912
	ds_read_b128 v[198:201], v153 offset:39936
	global_load_lds_dwordx4 v[202:203], off
	v_lshl_add_u64 v[202:203], s[38:39], 0, v[130:131]
	s_mov_b32 m0, s50
	s_nop 0
	global_load_lds_dwordx4 v[202:203], off
	s_waitcnt lgkmcnt(8)
	s_barrier
	s_waitcnt lgkmcnt(0)
	s_waitcnt lgkmcnt(0)
	v_mfma_f32_16x16x32_bf16 v[126:129], v[144:147], v[170:173], v[126:129]
	v_mfma_f32_16x16x32_bf16 v[122:125], v[162:165], v[170:173], v[122:125]
	v_mfma_f32_16x16x32_bf16 v[110:113], v[144:147], v[178:181], v[110:113]
	v_mfma_f32_16x16x32_bf16 v[106:109], v[162:165], v[178:181], v[106:109]
	v_mfma_f32_16x16x32_bf16 v[94:97], v[144:147], v[186:189], v[94:97]
	v_mfma_f32_16x16x32_bf16 v[90:93], v[162:165], v[186:189], v[90:93]
	v_mfma_f32_16x16x32_bf16 v[78:81], v[144:147], v[194:197], v[78:81]
	v_mfma_f32_16x16x32_bf16 v[74:77], v[162:165], v[194:197], v[74:77]
	v_mfma_f32_16x16x32_bf16 v[126:129], v[158:161], v[174:177], v[126:129]
	v_mfma_f32_16x16x32_bf16 v[122:125], v[166:169], v[174:177], v[122:125]
	v_mfma_f32_16x16x32_bf16 v[110:113], v[158:161], v[182:185], v[110:113]
	v_mfma_f32_16x16x32_bf16 v[106:109], v[166:169], v[182:185], v[106:109]
	v_mfma_f32_16x16x32_bf16 v[94:97], v[158:161], v[190:193], v[94:97]
	v_mfma_f32_16x16x32_bf16 v[90:93], v[166:169], v[190:193], v[90:93]
	v_mfma_f32_16x16x32_bf16 v[78:81], v[158:161], v[198:201], v[78:81]
	v_mfma_f32_16x16x32_bf16 v[74:77], v[166:169], v[198:201], v[74:77]
	s_barrier
	s_add_i32 s38, 0, 0x1c000
	s_add_i32 s39, s70, s46
	v_add_u32_e32 v134, s38, v150
	v_lshl_add_u64 v[148:149], v[148:149], 0, s[6:7]
	s_mov_b32 m0, s39
	ds_read_b128 v[202:205], v134
	ds_read_b128 v[206:209], v134 offset:1024
	ds_read_b128 v[210:213], v134 offset:2048
	ds_read_b128 v[214:217], v134 offset:3072
	global_load_lds_dwordx4 v[148:149], off
	v_lshl_add_u64 v[148:149], v[218:219], 0, s[6:7]
	s_add_i32 m0, s39, 0x2000
	s_nop 0
	global_load_lds_dwordx4 v[148:149], off
	s_barrier
	s_waitcnt lgkmcnt(0)
	s_waitcnt lgkmcnt(0)
	v_mfma_f32_16x16x32_bf16 v[118:121], v[202:205], v[170:173], v[118:121]
	v_mfma_f32_16x16x32_bf16 v[114:117], v[210:213], v[170:173], v[114:117]
	v_mfma_f32_16x16x32_bf16 v[102:105], v[202:205], v[178:181], v[102:105]
	v_mfma_f32_16x16x32_bf16 v[98:101], v[210:213], v[178:181], v[98:101]
	v_mfma_f32_16x16x32_bf16 v[86:89], v[202:205], v[186:189], v[86:89]
	v_mfma_f32_16x16x32_bf16 v[82:85], v[210:213], v[186:189], v[82:85]
	v_mfma_f32_16x16x32_bf16 v[70:73], v[202:205], v[194:197], v[70:73]
	v_mfma_f32_16x16x32_bf16 v[66:69], v[210:213], v[194:197], v[66:69]
	v_mfma_f32_16x16x32_bf16 v[118:121], v[206:209], v[174:177], v[118:121]
	v_mfma_f32_16x16x32_bf16 v[114:117], v[214:217], v[174:177], v[114:117]
	v_mfma_f32_16x16x32_bf16 v[102:105], v[206:209], v[182:185], v[102:105]
	v_mfma_f32_16x16x32_bf16 v[98:101], v[214:217], v[182:185], v[98:101]
	v_mfma_f32_16x16x32_bf16 v[86:89], v[206:209], v[190:193], v[86:89]
	v_mfma_f32_16x16x32_bf16 v[82:85], v[214:217], v[190:193], v[82:85]
	v_mfma_f32_16x16x32_bf16 v[70:73], v[206:209], v[198:201], v[70:73]
	v_mfma_f32_16x16x32_bf16 v[66:69], v[214:217], v[198:201], v[66:69]
	s_mov_b32 m0, s52
	v_lshl_add_u64 v[148:149], v[220:221], 0, s[6:7]
	s_barrier
	ds_read_b128 v[170:173], v153 offset:49152
	ds_read_b128 v[174:177], v153 offset:50176
	ds_read_b128 v[178:181], v153 offset:51200
	ds_read_b128 v[182:185], v153 offset:52224
	ds_read_b128 v[186:189], v153 offset:53248
	ds_read_b128 v[190:193], v153 offset:54272
	ds_read_b128 v[194:197], v153 offset:55296
	ds_read_b128 v[198:201], v153 offset:56320
	global_load_lds_dwordx4 v[148:149], off
	v_lshl_add_u64 v[148:149], v[222:223], 0, s[6:7]
	s_mov_b32 m0, s53
	s_nop 0
	global_load_lds_dwordx4 v[148:149], off
	s_barrier
	s_waitcnt lgkmcnt(0)
	s_waitcnt lgkmcnt(0)
	v_mfma_f32_16x16x32_bf16 v[62:65], v[144:147], v[170:173], v[62:65]
	v_mfma_f32_16x16x32_bf16 v[58:61], v[162:165], v[170:173], v[58:61]
	v_mfma_f32_16x16x32_bf16 v[46:49], v[144:147], v[178:181], v[46:49]
	v_mfma_f32_16x16x32_bf16 v[42:45], v[162:165], v[178:181], v[42:45]
	v_mfma_f32_16x16x32_bf16 v[30:33], v[144:147], v[186:189], v[30:33]
	v_mfma_f32_16x16x32_bf16 v[26:29], v[162:165], v[186:189], v[26:29]
	v_mfma_f32_16x16x32_bf16 v[22:25], v[144:147], v[194:197], v[22:25]
	v_mfma_f32_16x16x32_bf16 v[14:17], v[162:165], v[194:197], v[14:17]
	v_mfma_f32_16x16x32_bf16 v[62:65], v[158:161], v[174:177], v[62:65]
	v_mfma_f32_16x16x32_bf16 v[58:61], v[166:169], v[174:177], v[58:61]
	v_mfma_f32_16x16x32_bf16 v[46:49], v[158:161], v[182:185], v[46:49]
	v_mfma_f32_16x16x32_bf16 v[42:45], v[166:169], v[182:185], v[42:45]
	v_mfma_f32_16x16x32_bf16 v[30:33], v[158:161], v[190:193], v[30:33]
	v_mfma_f32_16x16x32_bf16 v[26:29], v[166:169], v[190:193], v[26:29]
	v_mfma_f32_16x16x32_bf16 v[22:25], v[158:161], v[198:201], v[22:25]
	v_mfma_f32_16x16x32_bf16 v[14:17], v[166:169], v[198:201], v[14:17]
	s_barrier
	s_add_u32 s36, s36, 0x80080
	s_addc_u32 s37, s37, 0
	s_add_i32 s38, s38, s46
	v_lshl_add_u64 v[144:145], s[36:37], 0, v[132:133]
	s_mov_b32 m0, s38
	s_nop 0
	global_load_lds_dwordx4 v[144:145], off
	v_lshl_add_u64 v[144:145], s[36:37], 0, v[130:131]
	s_add_i32 m0, s38, 0x2000
	s_nop 0
	global_load_lds_dwordx4 v[144:145], off
	s_waitcnt vmcnt(6)
	s_barrier
	v_mfma_f32_16x16x32_bf16 v[54:57], v[202:205], v[170:173], v[54:57]
	v_mfma_f32_16x16x32_bf16 v[50:53], v[210:213], v[170:173], v[50:53]
	v_mfma_f32_16x16x32_bf16 v[38:41], v[202:205], v[178:181], v[38:41]
	v_mfma_f32_16x16x32_bf16 v[34:37], v[210:213], v[178:181], v[34:37]
	v_mfma_f32_16x16x32_bf16 v[18:21], v[202:205], v[186:189], v[18:21]
	v_mfma_f32_16x16x32_bf16 v[10:13], v[210:213], v[186:189], v[10:13]
	v_mfma_f32_16x16x32_bf16 v[6:9], v[202:205], v[194:197], v[6:9]
	v_mfma_f32_16x16x32_bf16 v[2:5], v[210:213], v[194:197], v[2:5]
	v_mfma_f32_16x16x32_bf16 v[54:57], v[206:209], v[174:177], v[54:57]
	v_mfma_f32_16x16x32_bf16 v[50:53], v[214:217], v[174:177], v[50:53]
	v_mfma_f32_16x16x32_bf16 v[38:41], v[206:209], v[182:185], v[38:41]
	v_mfma_f32_16x16x32_bf16 v[34:37], v[214:217], v[182:185], v[34:37]
	v_mfma_f32_16x16x32_bf16 v[18:21], v[206:209], v[190:193], v[18:21]
	v_mfma_f32_16x16x32_bf16 v[10:13], v[214:217], v[190:193], v[10:13]
	v_mfma_f32_16x16x32_bf16 v[6:9], v[206:209], v[198:201], v[6:9]
	v_mfma_f32_16x16x32_bf16 v[2:5], v[214:217], v[198:201], v[2:5]
	s_add_i32 s69, s69, 2
	s_add_u32 s34, s34, 0x100
	s_addc_u32 s35, s35, 0
	s_add_u32 s67, s67, 0x100
	s_addc_u32 s68, s68, 0
	s_cmp_gt_u32 s69, 29
	s_barrier
	s_cbranch_scc0 .LBB0_3319
	v_lshl_add_u32 v146, s30, 8, v1
	v_lshl_or_b32 v144, s64, 8, v151
	v_ashrrev_i32_e32 v147, 31, v146
	s_movk_i32 s23, 0x3fff
	v_ashrrev_i32_e32 v145, 31, v144
	v_lshlrev_b64 v[148:149], 13, v[146:147]
	v_cmp_lt_i32_e32 vcc, s23, v146
	v_lshl_add_u64 v[158:159], s[8:9], 0, v[148:149]
	v_lshlrev_b64 v[144:145], 2, v[144:145]
	v_cndmask_b32_e32 v134, v155, v156, vcc
	v_lshl_add_u64 v[174:175], v[158:159], 0, v[144:145]
	v_lshl_add_u64 v[158:159], s[4:5], 0, v[134:135]
	v_lshl_add_u64 v[166:167], v[158:159], 0, v[144:145]
	v_add_co_u32_e32 v162, vcc, s57, v166
	s_nop 1
	v_addc_co_u32_e32 v163, vcc, 0, v167, vcc
	v_lshl_add_u64 v[170:171], s[10:11], 0, v[148:149]
	v_lshl_add_u64 v[180:181], v[170:171], 0, v[144:145]
	v_lshl_add_u64 v[178:179], v[166:167], 0, s[12:13]
	global_load_dwordx4 v[144:147], v[162:163], off
	global_load_dwordx4 v[158:161], v[178:179], off offset:64
	global_load_dwordx4 v[164:167], v[178:179], off offset:512
	global_load_dwordx4 v[168:171], v[178:179], off offset:576
	global_load_dwordx4 v[182:185], v[174:175], off
	global_load_dwordx4 v[186:189], v[174:175], off offset:64
	global_load_dwordx4 v[190:193], v[174:175], off offset:512
	global_load_dwordx4 v[194:197], v[174:175], off offset:576
	v_add_co_u32_e32 v172, vcc, 0x20000, v174
	s_nop 1
	v_addc_co_u32_e32 v173, vcc, 0, v175, vcc
	global_load_dwordx4 v[198:201], v[172:173], off
	global_load_dwordx4 v[202:205], v[172:173], off offset:64
	global_load_dwordx4 v[206:209], v[172:173], off offset:512
	global_load_dwordx4 v[210:213], v[172:173], off offset:576
	v_add_co_u32_e32 v214, vcc, 0x20000, v180
	s_nop 1
	v_addc_co_u32_e32 v215, vcc, 0, v181, vcc
	s_waitcnt vmcnt(7)
	v_pk_fma_f32 v[128:129], v[128:129], v[146:147], v[184:185]
	v_pk_fma_f32 v[126:127], v[126:127], v[144:145], v[182:183]
	global_store_dwordx4 v[180:181], v[126:129], off
	s_waitcnt vmcnt(7)
	v_pk_fma_f32 v[124:125], v[124:125], v[160:161], v[188:189]
	v_pk_fma_f32 v[122:123], v[122:123], v[158:159], v[186:187]
	global_store_dwordx4 v[180:181], v[122:125], off offset:64
	s_waitcnt vmcnt(7)
	v_pk_fma_f32 v[120:121], v[120:121], v[166:167], v[192:193]
	v_pk_fma_f32 v[118:119], v[118:119], v[164:165], v[190:191]
	global_store_dwordx4 v[180:181], v[118:121], off offset:512
	s_waitcnt vmcnt(7)
	v_pk_fma_f32 v[116:117], v[116:117], v[170:171], v[196:197]
	v_pk_fma_f32 v[114:115], v[114:115], v[168:169], v[194:195]
	global_store_dwordx4 v[180:181], v[114:117], off offset:576
	s_waitcnt vmcnt(7)
	v_pk_fma_f32 v[112:113], v[112:113], v[146:147], v[200:201]
	v_pk_fma_f32 v[110:111], v[110:111], v[144:145], v[198:199]
	global_store_dwordx4 v[214:215], v[110:113], off
	s_waitcnt vmcnt(7)
	v_pk_fma_f32 v[108:109], v[108:109], v[160:161], v[204:205]
	v_pk_fma_f32 v[106:107], v[106:107], v[158:159], v[202:203]
	global_store_dwordx4 v[214:215], v[106:109], off offset:64
	s_waitcnt vmcnt(7)
	v_pk_fma_f32 v[104:105], v[104:105], v[166:167], v[208:209]
	v_pk_fma_f32 v[102:103], v[102:103], v[164:165], v[206:207]
	global_store_dwordx4 v[214:215], v[102:105], off offset:512
	s_waitcnt vmcnt(7)
	v_pk_fma_f32 v[100:101], v[100:101], v[170:171], v[212:213]
	v_pk_fma_f32 v[98:99], v[98:99], v[168:169], v[210:211]
	global_store_dwordx4 v[214:215], v[98:101], off offset:576
	v_add_co_u32_e32 v148, vcc, 0x40000, v174
	s_nop 1
	v_addc_co_u32_e32 v149, vcc, 0, v175, vcc
	global_load_dwordx4 v[182:185], v[148:149], off
	global_load_dwordx4 v[186:189], v[148:149], off offset:64
	global_load_dwordx4 v[190:193], v[148:149], off offset:512
	global_load_dwordx4 v[194:197], v[148:149], off offset:576
	v_add_co_u32_e32 v172, vcc, 0x60000, v174
	s_nop 1
	v_addc_co_u32_e32 v173, vcc, 0, v175, vcc
	global_load_dwordx4 v[198:201], v[172:173], off
	global_load_dwordx4 v[202:205], v[172:173], off offset:64
	global_load_dwordx4 v[206:209], v[172:173], off offset:512
	global_load_dwordx4 v[210:213], v[172:173], off offset:576
	v_add_co_u32_e32 v176, vcc, 0x40000, v180
	s_nop 1
	v_addc_co_u32_e32 v177, vcc, 0, v181, vcc
	v_add_co_u32_e32 v214, vcc, 0x60000, v180
	s_nop 1
	v_addc_co_u32_e32 v215, vcc, 0, v181, vcc
	s_waitcnt vmcnt(7)
	v_pk_fma_f32 v[96:97], v[96:97], v[146:147], v[184:185]
	v_pk_fma_f32 v[94:95], v[94:95], v[144:145], v[182:183]
	global_store_dwordx4 v[176:177], v[94:97], off
	s_waitcnt vmcnt(7)
	v_pk_fma_f32 v[92:93], v[92:93], v[160:161], v[188:189]
	v_pk_fma_f32 v[90:91], v[90:91], v[158:159], v[186:187]
	global_store_dwordx4 v[176:177], v[90:93], off offset:64
	s_waitcnt vmcnt(7)
	v_pk_fma_f32 v[88:89], v[88:89], v[166:167], v[192:193]
	v_pk_fma_f32 v[86:87], v[86:87], v[164:165], v[190:191]
	global_store_dwordx4 v[176:177], v[86:89], off offset:512
	s_waitcnt vmcnt(7)
	v_pk_fma_f32 v[84:85], v[84:85], v[170:171], v[196:197]
	v_pk_fma_f32 v[82:83], v[82:83], v[168:169], v[194:195]
	global_store_dwordx4 v[176:177], v[82:85], off offset:576
	s_waitcnt vmcnt(7)
	v_pk_fma_f32 v[80:81], v[80:81], v[146:147], v[200:201]
	v_pk_fma_f32 v[78:79], v[78:79], v[144:145], v[198:199]
	global_store_dwordx4 v[214:215], v[78:81], off
	s_waitcnt vmcnt(7)
	v_pk_fma_f32 v[76:77], v[76:77], v[160:161], v[204:205]
	v_pk_fma_f32 v[74:75], v[74:75], v[158:159], v[202:203]
	global_store_dwordx4 v[214:215], v[74:77], off offset:64
	s_waitcnt vmcnt(7)
	v_pk_fma_f32 v[72:73], v[72:73], v[166:167], v[208:209]
	v_pk_fma_f32 v[70:71], v[70:71], v[164:165], v[206:207]
	global_store_dwordx4 v[214:215], v[70:73], off offset:512
	s_waitcnt vmcnt(7)
	v_pk_fma_f32 v[68:69], v[68:69], v[170:171], v[212:213]
	v_pk_fma_f32 v[66:67], v[66:67], v[168:169], v[210:211]
	global_store_dwordx4 v[214:215], v[66:69], off offset:576
	v_add_co_u32_e32 v148, vcc, 0x100000, v174
	s_nop 1
	v_addc_co_u32_e32 v149, vcc, 0, v175, vcc
	global_load_dwordx4 v[182:185], v[148:149], off
	global_load_dwordx4 v[186:189], v[148:149], off offset:64
	global_load_dwordx4 v[190:193], v[148:149], off offset:512
	global_load_dwordx4 v[194:197], v[148:149], off offset:576
	v_add_co_u32_e32 v172, vcc, 0x120000, v174
	s_nop 1
	v_addc_co_u32_e32 v173, vcc, 0, v175, vcc
	global_load_dwordx4 v[198:201], v[172:173], off
	global_load_dwordx4 v[202:205], v[172:173], off offset:64
	global_load_dwordx4 v[206:209], v[172:173], off offset:512
	global_load_dwordx4 v[210:213], v[172:173], off offset:576
	v_add_co_u32_e32 v176, vcc, 0x100000, v180
	s_nop 1
	v_addc_co_u32_e32 v177, vcc, 0, v181, vcc
	v_add_co_u32_e32 v214, vcc, 0x120000, v180
	s_nop 1
	v_addc_co_u32_e32 v215, vcc, 0, v181, vcc
	s_waitcnt vmcnt(7)
	v_pk_fma_f32 v[64:65], v[64:65], v[146:147], v[184:185]
	v_pk_fma_f32 v[62:63], v[62:63], v[144:145], v[182:183]
	global_store_dwordx4 v[176:177], v[62:65], off
	s_waitcnt vmcnt(7)
	v_pk_fma_f32 v[60:61], v[60:61], v[160:161], v[188:189]
	v_pk_fma_f32 v[58:59], v[58:59], v[158:159], v[186:187]
	global_store_dwordx4 v[176:177], v[58:61], off offset:64
	s_waitcnt vmcnt(7)
	v_pk_fma_f32 v[56:57], v[56:57], v[166:167], v[192:193]
	v_pk_fma_f32 v[54:55], v[54:55], v[164:165], v[190:191]
	global_store_dwordx4 v[176:177], v[54:57], off offset:512
	s_waitcnt vmcnt(7)
	v_pk_fma_f32 v[52:53], v[52:53], v[170:171], v[196:197]
	v_pk_fma_f32 v[50:51], v[50:51], v[168:169], v[194:195]
	global_store_dwordx4 v[176:177], v[50:53], off offset:576
	s_waitcnt vmcnt(7)
	v_pk_fma_f32 v[48:49], v[48:49], v[146:147], v[200:201]
	v_pk_fma_f32 v[46:47], v[46:47], v[144:145], v[198:199]
	global_store_dwordx4 v[214:215], v[46:49], off
	s_waitcnt vmcnt(7)
	v_pk_fma_f32 v[44:45], v[44:45], v[160:161], v[204:205]
	v_pk_fma_f32 v[42:43], v[42:43], v[158:159], v[202:203]
	global_store_dwordx4 v[214:215], v[42:45], off offset:64
	s_waitcnt vmcnt(7)
	v_pk_fma_f32 v[40:41], v[40:41], v[166:167], v[208:209]
	v_pk_fma_f32 v[38:39], v[38:39], v[164:165], v[206:207]
	global_store_dwordx4 v[214:215], v[38:41], off offset:512
	s_waitcnt vmcnt(7)
	v_pk_fma_f32 v[36:37], v[36:37], v[170:171], v[212:213]
	v_pk_fma_f32 v[34:35], v[34:35], v[168:169], v[210:211]
	global_store_dwordx4 v[214:215], v[34:37], off offset:576
	v_add_co_u32_e32 v148, vcc, 0x140000, v174
	s_nop 1
	v_addc_co_u32_e32 v149, vcc, 0, v175, vcc
	global_load_dwordx4 v[182:185], v[148:149], off
	global_load_dwordx4 v[186:189], v[148:149], off offset:64
	global_load_dwordx4 v[190:193], v[148:149], off offset:512
	global_load_dwordx4 v[194:197], v[148:149], off offset:576
	v_add_co_u32_e32 v172, vcc, 0x160000, v174
	s_nop 1
	v_addc_co_u32_e32 v173, vcc, 0, v175, vcc
	global_load_dwordx4 v[198:201], v[172:173], off
	global_load_dwordx4 v[202:205], v[172:173], off offset:64
	global_load_dwordx4 v[206:209], v[172:173], off offset:512
	global_load_dwordx4 v[210:213], v[172:173], off offset:576
	v_add_co_u32_e32 v176, vcc, 0x140000, v180
	s_nop 1
	v_addc_co_u32_e32 v177, vcc, 0, v181, vcc
	v_add_co_u32_e32 v214, vcc, 0x160000, v180
	s_nop 1
	v_addc_co_u32_e32 v215, vcc, 0, v181, vcc
	s_waitcnt vmcnt(7)
	v_pk_fma_f32 v[32:33], v[32:33], v[146:147], v[184:185]
	v_pk_fma_f32 v[30:31], v[30:31], v[144:145], v[182:183]
	global_store_dwordx4 v[176:177], v[30:33], off
	s_waitcnt vmcnt(7)
	v_pk_fma_f32 v[28:29], v[28:29], v[160:161], v[188:189]
	v_pk_fma_f32 v[26:27], v[26:27], v[158:159], v[186:187]
	global_store_dwordx4 v[176:177], v[26:29], off offset:64
	s_waitcnt vmcnt(7)
	v_pk_fma_f32 v[20:21], v[20:21], v[166:167], v[192:193]
	v_pk_fma_f32 v[18:19], v[18:19], v[164:165], v[190:191]
	global_store_dwordx4 v[176:177], v[18:21], off offset:512
	s_waitcnt vmcnt(7)
	v_pk_fma_f32 v[12:13], v[12:13], v[170:171], v[196:197]
	v_pk_fma_f32 v[10:11], v[10:11], v[168:169], v[194:195]
	global_store_dwordx4 v[176:177], v[10:13], off offset:576
	s_waitcnt vmcnt(7)
	v_pk_fma_f32 v[24:25], v[24:25], v[146:147], v[200:201]
	v_pk_fma_f32 v[22:23], v[22:23], v[144:145], v[198:199]
	global_store_dwordx4 v[214:215], v[22:25], off
	s_waitcnt vmcnt(7)
	v_pk_fma_f32 v[16:17], v[16:17], v[160:161], v[204:205]
	v_pk_fma_f32 v[14:15], v[14:15], v[158:159], v[202:203]
	global_store_dwordx4 v[214:215], v[14:17], off offset:64
	s_waitcnt vmcnt(7)
	v_pk_fma_f32 v[8:9], v[8:9], v[166:167], v[208:209]
	v_pk_fma_f32 v[6:7], v[6:7], v[164:165], v[206:207]
	global_store_dwordx4 v[214:215], v[6:9], off offset:512
	s_waitcnt vmcnt(7)
	v_pk_fma_f32 v[4:5], v[4:5], v[170:171], v[212:213]
	v_pk_fma_f32 v[2:3], v[2:3], v[168:169], v[210:211]
	global_store_dwordx4 v[214:215], v[2:5], off offset:576
	s_mov_b32 s64, s22
	s_mov_b32 s30, s24
	s_mov_b64 s[36:37], s[28:29]
	s_mov_b64 s[34:35], s[26:27]
	s_and_b64 vcc, exec, s[0:1]
	s_cbranch_vccz .LBB0_3316
	s_waitcnt vmcnt(0)
	v_readlane_b32 s52, v250, 40
	s_cmpk_gt_u32 s41, 0xff
	v_readlane_b32 s53, v250, 41
	v_readlane_b32 s54, v250, 42
	v_readlane_b32 s55, v250, 43
	s_cbranch_scc1 .LBB0_3323
	s_barrier

.LBB0_3869:
	s_cmp_lt_i32 s54, 23
	s_cselect_b64 s[6:7], -1, 0
	s_and_b64 s[0:1], s[6:7], s[0:1]
	s_andn2_b64 vcc, exec, s[0:1]
	s_cbranch_vccnz .LBB0_3887
	v_mov_b32_e32 v1, v248
	s_waitcnt vmcnt(5)
	v_mov_b32_e32 v2, v0
	v_readlane_b32 s33, v250, 1
	v_readlane_b32 s36, v250, 0
	v_readlane_b32 s0, v250, 39
	s_mov_b64 s[2:3], s[90:91]
	s_mov_b64 s[0:1], s[52:53]
	s_cmpk_gt_i32 s36, 0x3ff
	v_readfirstlane_b32 s37, v0
	s_barrier
	s_cbranch_scc1 .LBB0_3886
	s_add_u32 s8, s0, 0x2ec40000
	s_addc_u32 s9, s1, 0
	s_add_u32 s38, s0, 0x16940000
	s_addc_u32 s39, s1, 0
	s_add_u32 s10, s0, 0x1674000
	s_addc_u32 s11, s1, 0
	s_ashr_i32 s41, s36, 31
	s_lshr_b32 s5, s41, 29
	s_add_i32 s5, s36, s5
	s_lshr_b32 s4, s37, 6
	s_ashr_i32 s12, s5, 3
	s_and_b32 s5, s5, -8
	s_lshr_b32 s3, s37, 8
	s_lshl_b32 s40, s4, 10
	s_sub_i32 s5, s36, s5
	s_cmp_lt_i32 s5, 0
	s_movk_i32 s42, 0x81
	s_cselect_b32 s13, s42, 0x80
	s_mul_i32 s5, s13, s5
	s_add_i32 s5, s5, s12
	s_ashr_i32 s12, s5, 31
	s_lshr_b32 s12, s12, 26
	s_add_i32 s12, s5, s12
	s_ashr_i32 s13, s12, 6
	s_lshl_b32 s14, s13, 3
	s_sub_i32 s13, 0x80, s14
	s_min_u32 s15, s13, 8
	s_andn2_b32 s12, s12, 63
	s_sub_i32 s5, s5, s12
	v_cvt_f32_ubyte0_e32 v5, s15
	v_cvt_f32_i32_e32 v4, s5
	s_waitcnt vmcnt(4)
	v_rcp_iflag_f32_e32 v6, v5
	v_bfe_u32 v2, v0, 2, 4
	v_lshrrev_b32_e32 v3, 3, v0
	v_and_or_b32 v1, v3, 48, v2
	v_or_b32_e32 v3, 64, v3
	s_movk_i32 s2, 0x70
	v_and_or_b32 v150, v3, s2, v2
	v_mul_f32_e32 v2, v4, v6
	v_trunc_f32_e32 v2, v2
	v_fma_f32 v3, -v2, v5, v4
	v_cvt_i32_f32_e32 v2, v2
	s_ashr_i32 s2, s5, 30
	s_or_b32 s2, s2, 1
	v_cmp_ge_f32_e64 s[12:13], |v3|, v5
	s_and_b64 s[12:13], s[12:13], exec
	s_cselect_b32 s2, s2, 0
	v_readfirstlane_b32 s12, v2
	s_add_i32 s2, s12, s2
	s_mul_i32 s12, s2, s15
	s_sub_i32 s5, s5, s12
	s_sext_i32_i8 s5, s5
	s_add_i32 s58, s14, s5
	s_lshr_b32 s5, s58, 29
	s_add_i32 s5, s58, s5
	s_ashr_i32 s12, s5, 3
	s_lshl_b32 s13, s12, 11
	s_lshl_b32 s14, s58, 8
	s_mul_i32 s5, s12, 0x900
	s_sub_i32 s13, s14, s13
	s_add_i32 s5, s13, s5
	v_or_b32_e32 v2, s5, v1
	v_or_b32_e32 v4, s5, v150
	s_bitset1_b32 s5, 7
	v_ashrrev_i32_e32 v3, 31, v2
	v_or_b32_e32 v6, s5, v1
	v_or_b32_e32 v8, s5, v150
	v_lshl_add_u64 v[2:3], v[2:3], 2, s[10:11]
	v_ashrrev_i32_e32 v5, 31, v4
	v_ashrrev_i32_e32 v7, 31, v6
	v_ashrrev_i32_e32 v9, 31, v8
	v_lshl_add_u64 v[4:5], v[4:5], 2, s[10:11]
	v_lshl_add_u64 v[6:7], v[6:7], 2, s[10:11]
	v_lshl_add_u64 v[8:9], v[8:9], 2, s[10:11]
	global_load_dword v10, v[2:3], off
	global_load_dword v11, v[4:5], off
	global_load_dword v12, v[6:7], off
	global_load_dword v13, v[8:9], off
	s_bfe_i64 s[14:15], s[2:3], 0x80000
	s_ashr_i32 s13, s12, 31
	s_lshl_b64 s[14:15], s[14:15], 20
	s_lshl_b64 s[12:13], s[12:13], 23
	s_add_u32 s5, s38, s12
	v_lshlrev_b32_e32 v2, 4, v0
	v_and_b32_e32 v3, 32, v0
	s_addc_u32 s12, s39, s13
	v_bitop3_b32 v2, v2, v3, 48 bitop3:0x6c
	s_add_u32 s28, s5, s14
	v_and_or_b32 v151, v0, 64, v2
	s_addc_u32 s29, s12, s15
	s_add_i32 s43, s40, 0
	v_lshl_or_b32 v132, v1, 12, v151
	s_add_i32 m0, s43, 0x10000
	v_lshl_or_b32 v130, v150, 12, v151
	global_load_lds_dwordx4 v132, s[28:29]
	s_add_i32 m0, s43, 0x12000
	s_add_i32 s44, s43, 0x2000
	global_load_lds_dwordx4 v130, s[28:29]
	s_mov_b32 m0, s43
	s_add_u32 s12, s28, 0x80000
	s_addc_u32 s13, s29, 0
	s_add_i32 s45, s43, 0x4000
	s_add_i32 s46, s43, 0x6000
	v_mov_b32_e32 v135, 0
	v_mov_b32_e32 v133, v135
	v_mov_b32_e32 v131, v135
	s_mov_b32 s47, 0
	v_lshl_add_u64 v[4:5], s[28:29], 0, v[132:133]
	v_lshl_add_u64 v[2:3], s[28:29], 0, v[130:131]
	v_mov_b32_e32 v141, v135
	s_waitcnt vmcnt(0)
	v_lshl_or_b32 v134, v10, 12, v151
	v_lshl_or_b32 v140, v11, 12, v151
	global_load_lds_dwordx4 v134, s[8:9]
	s_mov_b32 m0, s44
	v_lshl_or_b32 v142, v12, 12, v151
	global_load_lds_dwordx4 v140, s[8:9]
	s_add_i32 m0, s43, 0x14000
	v_lshl_or_b32 v144, v13, 12, v151
	global_load_lds_dwordx4 v132, s[12:13]
	s_add_i32 m0, s43, 0x16000
	s_cmp_lg_u32 s3, 1
	global_load_lds_dwordx4 v130, s[12:13]
	s_mov_b32 m0, s45
	s_nop 0
	global_load_lds_dwordx4 v142, s[8:9]
	s_mov_b32 m0, s46
	s_nop 0
	global_load_lds_dwordx4 v144, s[8:9]
	s_cbranch_scc1 .LBB0_3873
	s_barrier
	s_setprio 1

.LBB0_3937:
	s_cmp_lt_i32 s54, 24
	s_cselect_b64 s[6:7], -1, 0
	s_and_b64 s[0:1], s[6:7], s[0:1]
	s_andn2_b64 vcc, exec, s[0:1]
	s_cbranch_vccnz .LBB0_3955
	v_mov_b32_e32 v1, v0
	s_waitcnt vmcnt(5)
	v_mov_b32_e32 v2, v248
	v_readlane_b32 s28, v250, 0
	v_readlane_b32 s0, v250, 39
	v_readlane_b32 s29, v250, 1
	s_mov_b64 s[2:3], s[90:91]
	s_mov_b64 s[0:1], s[52:53]
	s_cmpk_gt_i32 s28, 0x3ff
	v_readfirstlane_b32 s30, v0
	s_barrier
	s_cbranch_scc1 .LBB0_3954
	v_lshlrev_b32_e32 v1, 4, v0
	v_or_b32_e32 v10, 0x2000, v1
	v_and_b32_e32 v4, 32, v0
	v_lshrrev_b32_e32 v2, 7, v10
	v_bfe_u32 v13, v0, 2, 4
	s_movk_i32 s2, 0x70
	v_bitop3_b32 v11, v1, v4, 48 bitop3:0x6c
	v_and_b32_e32 v12, 64, v0
	s_add_u32 s31, s0, 0x32d40000
	v_and_or_b32 v3, v2, s2, v13
	v_or_b32_e32 v1, v11, v12
	s_addc_u32 s33, s1, 0
	v_lshl_or_b32 v130, v3, 11, v1
	v_lshrrev_b32_e32 v3, 5, v0
	v_lshrrev_b32_e32 v5, 1, v0
	s_add_u32 s34, s0, 0x1e940000
	v_and_b32_e32 v3, 4, v3
	v_bfe_u32 v4, v0, 2, 2
	v_and_b32_e32 v14, 24, v5
	s_addc_u32 s35, s1, 0
	v_or3_b32 v3, v3, v4, v14
	s_movk_i32 s2, 0x60
	s_ashr_i32 s37, s28, 31
	v_and_or_b32 v2, v2, s2, v3
	s_lshr_b32 s2, s37, 29
	s_add_i32 s2, s28, s2
	s_lshr_b32 s4, s30, 6
	s_ashr_i32 s5, s2, 3
	s_and_b32 s2, s2, -8
	s_lshr_b32 s3, s30, 8
	s_lshl_b32 s36, s4, 10
	s_sub_i32 s2, s28, s2
	s_cmp_lt_i32 s2, 0
	s_movk_i32 s38, 0x81
	s_cselect_b32 s8, s38, 0x80
	s_mul_i32 s2, s8, s2
	s_add_i32 s2, s2, s5
	s_ashr_i32 s5, s2, 31
	s_lshr_b32 s5, s5, 26
	s_add_i32 s5, s2, s5
	s_ashr_i32 s8, s5, 6
	s_lshl_b32 s10, s8, 3
	v_lshl_or_b32 v132, v2, 11, v1
	v_lshrrev_b32_e32 v2, 3, v0
	s_sub_i32 s8, 0x80, s10
	v_and_or_b32 v4, v2, 48, v13
	s_min_u32 s11, s8, 8
	s_andn2_b32 s5, s5, 63
	v_lshl_or_b32 v134, v4, 11, v1
	s_sub_i32 s5, s2, s5
	v_cvt_f32_ubyte0_e32 v4, s11
	v_and_or_b32 v2, v2, 32, v3
	v_cvt_f32_i32_e32 v3, s5
	v_rcp_iflag_f32_e32 v5, v4
	v_lshl_or_b32 v136, v2, 11, v1
	s_ashr_i32 s2, s5, 30
	s_or_b32 s2, s2, 1
	v_mul_f32_e32 v1, v3, v5
	v_trunc_f32_e32 v1, v1
	v_fma_f32 v2, -v1, v4, v3
	v_cvt_i32_f32_e32 v1, v1
	v_cmp_ge_f32_e64 s[8:9], |v2|, v4
	s_and_b64 s[8:9], s[8:9], exec
	s_cselect_b32 s2, s2, 0
	v_readfirstlane_b32 s8, v1
	s_add_i32 s2, s8, s2
	s_mul_i32 s8, s2, s11
	s_sub_i32 s5, s5, s8
	s_sext_i32_i8 s5, s5
	s_add_i32 s54, s10, s5
	s_lshr_b32 s5, s54, 29
	s_add_i32 s5, s54, s5
	s_ashr_i32 s8, s5, 3
	s_lshl_b32 s9, s54, 8
	s_lshl_b32 s10, s8, 11
	s_mul_i32 s5, s8, 0x900
	s_sub_i32 s9, s9, s10
	s_add_i32 s10, s9, s5
	s_ashr_i32 s11, s10, 31
	s_lshl_b64 s[10:11], s[10:11], 11
	s_add_u32 s22, s31, s10
	s_addc_u32 s23, s33, s11
	s_ashr_i32 s9, s8, 31
	s_bfe_i64 s[10:11], s[2:3], 0x80000
	s_lshl_b64 s[10:11], s[10:11], 19
	s_lshl_b64 s[8:9], s[8:9], 22
	s_add_u32 s5, s34, s8
	s_addc_u32 s8, s35, s9
	s_add_u32 s24, s5, s10
	s_addc_u32 s25, s8, s11
	s_add_i32 s39, s36, 0
	s_add_i32 m0, s39, 0x10000
	s_add_i32 s40, s39, 0x2000
	global_load_lds_dwordx4 v136, s[24:25]
	s_add_i32 m0, s39, 0x12000
	s_add_u32 s8, s24, 0x40000
	global_load_lds_dwordx4 v132, s[24:25]
	s_mov_b32 m0, s39
	s_addc_u32 s9, s25, 0
	global_load_lds_dwordx4 v134, s[22:23]
	s_mov_b32 m0, s40
	v_mov_b32_e32 v137, 0
	global_load_lds_dwordx4 v130, s[22:23]
	s_add_i32 m0, s39, 0x14000
	v_mov_b32_e32 v133, v137
	global_load_lds_dwordx4 v136, s[8:9]
	s_add_i32 m0, s39, 0x16000
	v_mov_b32_e32 v135, v137
	global_load_lds_dwordx4 v132, s[8:9]
	s_add_u32 s8, s22, 0x40000
	s_addc_u32 s9, s23, 0
	s_add_i32 s41, s39, 0x4000
	s_mov_b32 m0, s41
	s_add_i32 s42, s39, 0x6000
	global_load_lds_dwordx4 v134, s[8:9]
	s_mov_b32 m0, s42
	v_mov_b32_e32 v131, v137
	global_load_lds_dwordx4 v130, s[8:9]
	s_mov_b32 s43, 0
	s_waitcnt vmcnt(0)
	v_lshl_add_u64 v[8:9], s[24:25], 0, v[136:137]
	v_lshl_add_u64 v[6:7], s[24:25], 0, v[132:133]
	v_lshl_add_u64 v[4:5], s[22:23], 0, v[134:135]
	s_cmp_lg_u32 s3, 1
	v_lshl_add_u64 v[2:3], s[22:23], 0, v[130:131]
	s_cbranch_scc1 .LBB0_3941
	s_barrier
	s_setprio 1
